# speedup vs baseline: 1.0080x; 1.0080x over previous
.LBB0_8:
	s_or_b64 exec, exec, s[4:5]
	v_lshrrev_b32_e32 v3, 4, v3
	v_and_b32_e32 v3, 0xfffffc0, v3
	v_and_b32_e32 v8, 48, v0
	v_and_b32_e32 v2, 15, v2
	v_or3_b32 v2, v8, v3, v2
	v_and_b32_e32 v3, 15, v0
	v_lshl_or_b32 v2, v2, 4, v3
	v_mul_f32_e32 v3, v7, v7
	v_mov_b32_e32 v8, 0x3c0881c4
	v_fmac_f32_e32 v8, 0xb94c1982, v3
	v_fmaak_f32 v8, v3, v8, 0xbe2aaa9d
	v_mul_f32_e32 v8, v3, v8
	v_fmac_f32_e32 v7, v7, v8
	v_mov_b32_e32 v8, 0xbab64f3b
	v_fmac_f32_e32 v8, 0x37d75334, v3
	v_fmaak_f32 v8, v3, v8, 0x3d2aabf7
	v_fmaak_f32 v8, v3, v8, 0xbf000004
	v_fma_f32 v3, v3, v8, 1.0
	v_and_b32_e32 v8, 1, v6
	v_cmp_eq_u32_e32 vcc, 0, v8
	s_load_dwordx2 s[12:13], s[0:1], 0x48
	v_lshlrev_b32_e32 v6, 30, v6
	v_cndmask_b32_e64 v3, -v7, v3, vcc
	s_brev_b32 s3, 1
	v_bitop3_b32 v3, v6, v3, s3 bitop3:0x6c
	s_movk_i32 s3, 0x1f8
	v_mov_b32_e32 v6, 0x7fc00000
	v_cmp_class_f32_e64 vcc, v1, s3
	s_nop 1
	v_cndmask_b32_e32 v8, v6, v3, vcc
	v_mov_b32_e32 v3, 0
	s_waitcnt lgkmcnt(0)
	v_lshl_add_u64 v[6:7], v[2:3], 2, s[10:11]
	global_store_dword v[6:7], v8, off sc1
	s_and_saveexec_b64 s[4:5], s[14:15]
	s_xor_b64 s[14:15], exec, s[4:5]
	s_cbranch_execz .LBB0_10
	v_add_u32_e32 v5, 0xffffff88, v5
	v_not_b32_e32 v6, 63
	v_cmp_lt_u32_e64 s[4:5], 63, v5
	s_mov_b32 s3, 0xfe5163ab
	v_mov_b32_e32 v9, v3
	v_cndmask_b32_e64 v6, 0, v6, s[4:5]
	v_add_u32_e32 v5, v6, v5
	v_not_b32_e32 v6, 31
	v_cmp_lt_u32_e64 s[6:7], 31, v5
	v_mov_b32_e32 v11, v3
	v_mov_b32_e32 v13, v3
	v_cndmask_b32_e64 v7, 0, v6, s[6:7]
	v_add_u32_e32 v5, v7, v5
	v_cmp_lt_u32_e64 s[8:9], 31, v5
	v_mov_b32_e32 v15, v3
	v_mov_b32_e32 v17, v3
	v_cndmask_b32_e64 v6, 0, v6, s[8:9]
	v_add_u32_e32 v5, v6, v5
	v_and_b32_e32 v6, 0x7fffff, v4
	v_or_b32_e32 v20, 0x800000, v6
	v_mad_u64_u32 v[6:7], s[10:11], v20, s3, 0
	v_mov_b32_e32 v8, v7
	s_mov_b32 s3, 0x3c439041
	v_mad_u64_u32 v[8:9], s[10:11], v20, s3, v[8:9]
	v_mov_b32_e32 v10, v9
	s_mov_b32 s3, 0xdb629599
	v_mad_u64_u32 v[10:11], s[10:11], v20, s3, v[10:11]
	v_mov_b32_e32 v12, v11
	s_mov_b32 s3, 0xf534ddc0
	v_mad_u64_u32 v[12:13], s[10:11], v20, s3, v[12:13]
	v_mov_b32_e32 v14, v13
	s_mov_b32 s3, 0xfc2757d1
	v_mad_u64_u32 v[14:15], s[10:11], v20, s3, v[14:15]
	v_mov_b32_e32 v16, v15
	s_mov_b32 s3, 0x4e441529
	v_mad_u64_u32 v[16:17], s[10:11], v20, s3, v[16:17]
	v_mov_b32_e32 v18, v17
	v_mov_b32_e32 v19, v3
	s_mov_b32 s3, 0xa2f9836e
	v_mad_u64_u32 v[18:19], s[10:11], v20, s3, v[18:19]
	v_cndmask_b32_e64 v7, v16, v12, s[4:5]
	v_cndmask_b32_e64 v9, v18, v14, s[4:5]
	v_cndmask_b32_e64 v13, v19, v16, s[4:5]
	v_cndmask_b32_e64 v11, v9, v7, s[6:7]
	v_cndmask_b32_e64 v9, v13, v9, s[6:7]
	v_cndmask_b32_e64 v13, v14, v10, s[4:5]
	v_cndmask_b32_e64 v7, v7, v13, s[6:7]
	v_cndmask_b32_e64 v9, v9, v11, s[8:9]
	v_cndmask_b32_e64 v11, v11, v7, s[8:9]
	v_sub_u32_e32 v14, 32, v5
	v_alignbit_b32 v15, v9, v11, v14
	v_cmp_eq_u32_e64 s[10:11], 0, v5
	v_cndmask_b32_e64 v8, v12, v8, s[4:5]
	v_cndmask_b32_e64 v6, v10, v6, s[4:5]
	v_cndmask_b32_e64 v5, v15, v9, s[10:11]
	v_cndmask_b32_e64 v9, v13, v8, s[6:7]
	v_cndmask_b32_e64 v7, v7, v9, s[8:9]
	v_alignbit_b32 v12, v11, v7, v14
	v_cndmask_b32_e64 v11, v12, v11, s[10:11]
	v_bfe_u32 v15, v5, 29, 1
	v_cndmask_b32_e64 v6, v8, v6, s[6:7]
	v_alignbit_b32 v12, v5, v11, 30
	v_sub_u32_e32 v16, 0, v15
	v_cndmask_b32_e64 v6, v9, v6, s[8:9]
	v_xor_b32_e32 v12, v12, v16
	v_alignbit_b32 v8, v7, v6, v14
	v_cndmask_b32_e64 v7, v8, v7, s[10:11]
	v_ffbh_u32_e32 v9, v12
	v_alignbit_b32 v8, v11, v7, 30
	v_min_u32_e32 v9, 32, v9
	v_alignbit_b32 v6, v7, v6, 30
	v_xor_b32_e32 v8, v8, v16
	v_sub_u32_e32 v10, 31, v9
	v_xor_b32_e32 v6, v6, v16
	v_alignbit_b32 v11, v12, v8, v10
	v_alignbit_b32 v6, v8, v6, v10
	v_alignbit_b32 v7, v11, v6, 9
	v_ffbh_u32_e32 v8, v7
	v_min_u32_e32 v8, 32, v8
	v_lshrrev_b32_e32 v13, 29, v5
	v_not_b32_e32 v10, v8
	v_alignbit_b32 v6, v7, v6, v10
	v_lshlrev_b32_e32 v7, 31, v13
	v_or_b32_e32 v10, 0x33000000, v7
	v_add_lshl_u32 v8, v8, v9, 23
	v_lshrrev_b32_e32 v6, 9, v6
	v_sub_u32_e32 v8, v10, v8
	v_or_b32_e32 v7, 0.5, v7
	v_lshlrev_b32_e32 v9, 23, v9
	v_or_b32_e32 v6, v8, v6
	v_lshrrev_b32_e32 v8, 9, v11
	v_sub_u32_e32 v7, v7, v9
	v_or_b32_e32 v7, v8, v7
	s_mov_b32 s3, 0x3fc90fda
	v_mul_f32_e32 v8, 0x3fc90fda, v7
	v_fma_f32 v9, v7, s3, -v8
	v_fmamk_f32 v7, v7, 0x33a22168, v9
	v_fmac_f32_e32 v7, 0x3fc90fda, v6
	v_lshrrev_b32_e32 v5, 30, v5
	v_add_f32_e32 v7, v8, v7
	v_add_u32_e32 v6, v15, v5

.LBB0_12:
	s_or_b64 exec, exec, s[4:5]
	v_mul_f32_e32 v5, v7, v7
	v_mov_b32_e32 v8, 0x3c0881c4
	v_fmac_f32_e32 v8, 0xb94c1982, v5
	v_fmaak_f32 v8, v5, v8, 0xbe2aaa9d
	v_mul_f32_e32 v8, v5, v8
	v_fmac_f32_e32 v7, v7, v8
	v_mov_b32_e32 v8, 0xbab64f3b
	v_fmac_f32_e32 v8, 0x37d75334, v5
	v_fmaak_f32 v8, v5, v8, 0x3d2aabf7
	v_fmaak_f32 v8, v5, v8, 0xbf000004
	v_fma_f32 v5, v5, v8, 1.0
	v_and_b32_e32 v8, 1, v6
	v_lshlrev_b32_e32 v6, 30, v6
	v_cmp_eq_u32_e64 s[4:5], 0, v8
	v_and_b32_e32 v6, 0x80000000, v6
	v_xor_b32_e32 v1, v4, v1
	v_cndmask_b32_e64 v5, v5, v7, s[4:5]
	v_xor_b32_e32 v1, v1, v6
	v_xor_b32_e32 v1, v1, v5
	v_mov_b32_e32 v4, 0x7fc00000
	v_cndmask_b32_e32 v1, v4, v1, vcc
	v_lshl_add_u64 v[2:3], v[2:3], 2, s[12:13]
	global_store_dword v[2:3], v1, off sc1
	s_mov_b64 s[4:5], 0

.LBB0_24:
	s_lshl_b32 s6, s12, 6
	s_mov_b32 s7, 0
	s_lshl_b32 s11, s13, 6
	s_lshl_b64 s[14:15], s[6:7], 2
	v_lshrrev_b32_e32 v1, 4, v0
	s_waitcnt lgkmcnt(0)
	s_add_u32 s8, s8, s14
	v_lshlrev_b32_e32 v20, 4, v0
	s_addc_u32 s9, s9, s15
	v_and_b32_e32 v18, 0xf0, v20
	v_mov_b32_e32 v19, 0
	v_or_b32_e32 v16, s11, v1
	v_lshl_add_u64 v[14:15], s[8:9], 0, v[18:19]
	v_mad_u64_u32 v[2:3], s[8:9], s10, v16, 0
	v_lshl_add_u64 v[10:11], v[2:3], 2, v[14:15]
	v_or_b32_e32 v2, 16, v16
	v_mad_u64_u32 v[2:3], s[8:9], s10, v2, 0
	v_lshl_add_u64 v[12:13], v[2:3], 2, v[14:15]
	global_load_dwordx4 v[2:5], v[10:11], off nt
	global_load_dwordx4 v[6:9], v[12:13], off nt
	v_or_b32_e32 v10, 32, v16
	v_mad_u64_u32 v[10:11], s[8:9], s10, v10, 0
	v_lshl_add_u64 v[10:11], v[10:11], 2, v[14:15]
	v_or_b32_e32 v16, 48, v16
	global_load_dwordx4 v[10:13], v[10:11], off nt
	v_mad_u64_u32 v[16:17], s[8:9], s10, v16, 0
	v_lshl_add_u64 v[14:15], v[16:17], 2, v[14:15]
	global_load_dwordx4 v[14:17], v[14:15], off nt
	v_lshlrev_b32_e32 v21, 3, v0
	s_movk_i32 s7, 0x104
	v_and_b32_e32 v23, 56, v21
	v_lshrrev_b32_e32 v22, 3, v0
	v_mad_u32_u24 v1, v1, s7, v18
	v_or_b32_e32 v18, s11, v23
	v_mul_u32_u24_e32 v23, 0x41, v23
	s_and_b32 s6, s6, 0xf80
	v_and_b32_e32 v25, 48, v20
	v_lshlrev_b32_e32 v20, 1, v22
	v_lshrrev_b32_e32 v33, 5, v18
	v_lshlrev_b32_e32 v18, 2, v23
	s_lshl_b32 s7, s12, 4
	s_add_i32 s6, s6, s3
	v_lshl_add_u32 v34, v22, 2, v18
	s_and_b32 s3, s7, 16
	v_and_or_b32 v18, v20, 32, s6
	v_bfe_u32 v24, v0, 3, 4
	s_movk_i32 s8, 0x60
	v_or_b32_e32 v18, s3, v18
	v_bitop3_b32 v26, v20, s8, 64 bitop3:0xc8
	v_or_b32_e32 v20, v18, v24
	v_lshlrev_b32_e32 v18, 2, v18
	v_add_u32_e32 v27, 0x1040, v1
	v_add_u32_e32 v28, 0x1048, v1
	v_add_u32_e32 v29, 0x2080, v1
	v_add_u32_e32 v30, 0x2088, v1
	v_add_u32_e32 v31, 0x30c0, v1
	v_add_u32_e32 v32, 0x30c8, v1
	v_add_u32_e32 v35, 0x400, v34
	v_lshlrev_b32_e32 v22, 6, v20
	v_lshlrev_b32_e32 v20, 2, v20
	v_and_b32_e32 v18, 0x7fffffc0, v18
	v_and_b32_e32 v22, 0x3c0, v22
	v_and_b32_e32 v20, 32, v20
	v_add_u32_e32 v18, v18, v33
	v_bitop3_b32 v20, v22, v20, v25 bitop3:0x36
	v_lshlrev_b64 v[22:23], 10, v[18:19]
	v_mov_b32_e32 v21, v19
	v_lshl_add_u64 v[22:23], s[4:5], 0, v[22:23]
	v_or_b32_e32 v26, s6, v26
	s_waitcnt vmcnt(3)
	ds_write2_b32 v1, v2, v3 offset1:1
	ds_write2_b32 v1, v4, v5 offset0:2 offset1:3
	s_waitcnt vmcnt(2)
	ds_write2_b32 v27, v6, v7 offset1:1
	ds_write2_b32 v28, v8, v9 offset1:1
	s_waitcnt vmcnt(1)
	ds_write2_b32 v29, v10, v11 offset1:1
	ds_write2_b32 v30, v12, v13 offset1:1
	s_waitcnt vmcnt(0)
	ds_write2_b32 v31, v14, v15 offset1:1
	ds_write2_b32 v32, v16, v17 offset1:1
	s_waitcnt lgkmcnt(0)
	s_barrier
	ds_read2_b32 v[2:3], v34 offset1:65
	ds_read2_b32 v[4:5], v34 offset0:130 offset1:195
	ds_read2_b32 v[6:7], v35 offset0:4 offset1:69
	ds_read2_b32 v[8:9], v35 offset0:134 offset1:199
	v_lshl_add_u64 v[10:11], v[22:23], 0, v[20:21]
	s_waitcnt lgkmcnt(3)
	v_cvt_pk_f16_f32 v2, v2, v3
	s_waitcnt lgkmcnt(2)
	v_cvt_pk_f16_f32 v3, v4, v5
	s_waitcnt lgkmcnt(1)
	v_cvt_pk_f16_f32 v4, v6, v7
	s_waitcnt lgkmcnt(0)
	v_cvt_pk_f16_f32 v5, v8, v9
	global_store_dwordx4 v[10:11], v[2:5], off sc1
	ds_read2_b32 v[2:3], v34 offset0:32 offset1:97
	ds_read2_b32 v[4:5], v34 offset0:162 offset1:227
	ds_read2_b32 v[6:7], v35 offset0:36 offset1:101
	ds_read2_b32 v[8:9], v35 offset0:166 offset1:231
	v_or_b32_e32 v1, s3, v26
	v_or_b32_e32 v10, v1, v24
	v_lshlrev_b32_e32 v1, 2, v1
	v_and_b32_e32 v1, 0x7fffffc0, v1
	s_waitcnt lgkmcnt(3)
	v_cvt_pk_f16_f32 v2, v2, v3
	s_waitcnt lgkmcnt(2)
	v_cvt_pk_f16_f32 v3, v4, v5
	s_waitcnt lgkmcnt(1)
	v_cvt_pk_f16_f32 v4, v6, v7
	v_lshlrev_b32_e32 v6, 6, v10
	v_lshlrev_b32_e32 v7, 2, v10
	v_add_u32_e32 v18, v1, v33
	s_waitcnt lgkmcnt(0)
	v_cvt_pk_f16_f32 v5, v8, v9
	v_and_b32_e32 v6, 0x3c0, v6
	v_and_b32_e32 v7, 32, v7
	v_lshlrev_b64 v[8:9], 10, v[18:19]
	v_bitop3_b32 v6, v6, v7, v25 bitop3:0x36
	v_mov_b32_e32 v7, v19
	v_lshl_add_u64 v[8:9], s[4:5], 0, v[8:9]
	v_lshl_add_u64 v[6:7], v[8:9], 0, v[6:7]
	global_store_dwordx4 v[6:7], v[2:5], off sc1
	s_cbranch_execnz .LBB0_2
.LBB0_25:
	s_load_dwordx2 s[6:7], s[0:1], 0x0
	s_load_dwordx2 s[4:5], s[0:1], 0x28
	s_lshl_b32 s0, s2, 3
	v_lshrrev_b32_e32 v1, 6, v0
	v_or_b32_e32 v20, s0, v1
	v_lshrrev_b32_e32 v1, 2, v0
	v_lshlrev_b32_e32 v2, 3, v0
	s_ashr_i32 s0, s0, 2
	v_and_b32_e32 v17, 24, v2
	v_bfi_b32 v2, -16, s0, v1
	v_lshlrev_b32_e32 v1, 5, v20
	v_and_b32_e32 v1, 0x760, v1
	v_ashrrev_i32_e32 v3, 31, v2
	v_or_b32_e32 v4, v1, v17
	v_lshlrev_b64 v[2:3], 13, v[2:3]
	s_waitcnt lgkmcnt(0)
	v_lshl_add_u64 v[10:11], s[6:7], 0, v[2:3]
	v_lshlrev_b32_e32 v14, 2, v4
	v_mov_b32_e32 v15, 0
	v_lshl_add_u64 v[12:13], v[10:11], 0, v[14:15]
	v_or_b32_e32 v16, 4, v20
	s_movk_i32 s0, 0x7e0
	v_lshlrev_b32_e32 v32, 5, v16
	v_and_or_b32 v32, v32, s0, v17
	v_mov_b32_e32 v33, v15
	v_lshlrev_b32_e32 v32, 2, v32
	v_lshl_add_u64 v[18:19], v[10:11], 0, v[32:33]
	global_load_dwordx4 v[2:5], v[12:13], off nt
	global_load_dwordx4 v[6:9], v[12:13], off offset:16 nt
	global_load_dwordx4 v[24:27], v[18:19], off nt
	global_load_dwordx4 v[28:31], v[18:19], off offset:16 nt
	v_lshlrev_b32_e32 v17, 4, v0
	s_movk_i32 s0, 0xffc0
	v_and_b32_e32 v22, 48, v17
	v_ashrrev_i32_e32 v17, 31, v16
	v_bfe_u32 v14, v0, 2, 4
	v_and_b32_e32 v21, 32, v0
	v_lshlrev_b32_e32 v14, 6, v14
	v_bitop3_b32 v14, v14, v21, v22 bitop3:0x36
	v_lshrrev_b32_e32 v18, 5, v1
	v_lshlrev_b64 v[0:1], 10, v[16:17]
	v_and_or_b32 v16, v20, s0, v18
	v_ashrrev_i32_e32 v17, 31, v16
	v_lshl_add_u64 v[18:19], s[4:5], 0, v[0:1]
	v_lshlrev_b64 v[0:1], 10, v[16:17]
	v_lshl_add_u64 v[0:1], s[4:5], 0, v[0:1]
	v_lshl_add_u64 v[0:1], v[0:1], 0, v[14:15]
	v_lshl_add_u64 v[10:11], v[18:19], 0, v[14:15]
	s_waitcnt vmcnt(3)
	v_cvt_pk_f16_f32 v2, v2, v3
	v_cvt_pk_f16_f32 v3, v4, v5
	s_waitcnt vmcnt(2)
	v_cvt_pk_f16_f32 v4, v6, v7
	v_cvt_pk_f16_f32 v5, v8, v9
	global_store_dwordx4 v[0:1], v[2:5], off sc1
	s_waitcnt vmcnt(2)
	v_cvt_pk_f16_f32 v6, v24, v25
	v_cvt_pk_f16_f32 v7, v26, v27
	s_waitcnt vmcnt(1)
	v_cvt_pk_f16_f32 v8, v28, v29
	v_cvt_pk_f16_f32 v9, v30, v31
	global_store_dwordx4 v[10:11], v[6:9], off sc1
	s_endpgm

.LBB1_1:
	v_ashrrev_i32_e32 v3, 3, v165
	v_and_b32_e32 v17, -4, v3
	v_lshl_add_u32 v113, v17, 2, s92
	ds_read_b96 v[106:108], v113
	ds_read_b128 v[102:105], v113 offset:32
	ds_read_b96 v[110:112], v113 offset:128
	v_readlane_b32 s0, v248, 4
	s_or_b32 s1, s90, s0
	s_lshl_b32 s0, s33, 12
	s_add_i32 s0, s0, 0
	v_lshl_add_u32 v109, v16, 1, s0
	v_cndmask_b32_e64 v42, v42, v26, s[2:3]
	v_cndmask_b32_e64 v18, v34, v18, s[2:3]
	s_waitcnt lgkmcnt(0)
	v_mul_f32_e32 v26, v98, v110
	v_lshl_add_u32 v146, v17, 7, v109
	v_fma_mixlo_f16 v18, v18, v106, v26
	v_cndmask_b32_e64 v17, v67, v51, s[2:3]
	ds_write_b16 v146, v18 offset:32832
	v_mul_f32_e32 v18, v95, v111
	v_fma_mixlo_f16 v17, v17, v107, v18
	v_cndmask_b32_e64 v19, v35, v19, s[2:3]
	ds_write_b16 v146, v17 offset:32896
	v_mul_f32_e32 v17, v99, v111
	v_fma_mixlo_f16 v17, v19, v107, v17
	v_cndmask_b32_e64 v16, v68, v52, s[2:3]
	ds_write_b16 v146, v17 offset:32960
	v_mul_f32_e32 v17, v96, v112
	v_fma_mixlo_f16 v16, v16, v108, v17
	v_or_b32_e32 v3, 3, v3
	ds_write_b16 v146, v16 offset:33024
	v_lshl_add_u32 v16, v3, 2, s92
	ds_read2_b32 v[16:17], v16 offset1:32
	v_cndmask_b32_e64 v69, v69, v53, s[2:3]
	v_cndmask_b32_e64 v66, v66, v50, s[2:3]
	ds_read_b128 v[50:53], v113 offset:160
	v_cndmask_b32_e64 v20, v36, v20, s[2:3]
	v_mul_f32_e32 v18, v100, v112
	v_fma_mixlo_f16 v18, v20, v108, v18
	v_mul_f32_e32 v67, v94, v110
	v_cndmask_b32_e64 v21, v37, v21, s[2:3]
	ds_write_b16 v146, v18 offset:33088
	s_waitcnt lgkmcnt(0)
	v_mul_f32_e32 v18, v97, v17
	v_mul_f32_e32 v17, v101, v17
	v_fma_mixlo_f16 v66, v66, v106, v67
	v_lshl_add_u32 v3, v3, 7, v109
	v_fma_mixlo_f16 v18, v69, v16, v18
	v_fma_mixlo_f16 v16, v21, v16, v17
	v_cndmask_b32_e64 v54, v70, v54, s[2:3]
	ds_write_b16 v146, v66 offset:32768
	ds_write_b16 v3, v18 offset:32768
	ds_write_b16 v3, v16 offset:32832
	ds_read_b128 v[16:19], v113 offset:192
	v_mul_f32_e32 v3, v86, v50
	v_fma_mixlo_f16 v3, v54, v102, v3
	v_cndmask_b32_e64 v22, v38, v22, s[2:3]
	ds_write_b16 v146, v3 offset:33792
	v_mul_f32_e32 v3, v90, v50
	v_fma_mixlo_f16 v3, v22, v102, v3
	v_cndmask_b32_e64 v55, v71, v55, s[2:3]
	ds_write_b16 v146, v3 offset:33856
	v_mul_f32_e32 v3, v87, v51
	v_fma_mixlo_f16 v3, v55, v103, v3
	v_cndmask_b32_e64 v23, v39, v23, s[2:3]
	ds_write_b16 v146, v3 offset:33920
	v_mul_f32_e32 v3, v91, v51
	v_fma_mixlo_f16 v3, v23, v103, v3
	v_cndmask_b32_e64 v56, v72, v56, s[2:3]
	ds_write_b16 v146, v3 offset:33984
	v_mul_f32_e32 v3, v88, v52
	v_fma_mixlo_f16 v3, v56, v104, v3
	v_cndmask_b32_e64 v24, v40, v24, s[2:3]
	ds_write_b16 v146, v3 offset:34048
	v_mul_f32_e32 v3, v92, v52
	v_fma_mixlo_f16 v3, v24, v104, v3
	v_cndmask_b32_e64 v57, v73, v57, s[2:3]
	ds_write_b16 v146, v3 offset:34112
	v_mul_f32_e32 v3, v89, v53
	ds_read_b128 v[20:23], v113 offset:64
	v_fma_mixlo_f16 v3, v57, v105, v3
	v_cndmask_b32_e64 v25, v41, v25, s[2:3]
	ds_write_b16 v146, v3 offset:34176
	v_mul_f32_e32 v3, v93, v53
	v_fma_mixlo_f16 v3, v25, v105, v3
	v_cndmask_b32_e64 v58, v74, v58, s[2:3]
	ds_write_b16 v146, v3 offset:34240
	s_waitcnt lgkmcnt(0)
	v_mul_f32_e32 v3, v12, v16
	v_cndmask_b32_e64 v47, v47, v31, s[2:3]
	v_cndmask_b32_e64 v46, v46, v30, s[2:3]
	v_cndmask_b32_e64 v45, v45, v29, s[2:3]
	v_cndmask_b32_e64 v44, v44, v28, s[2:3]
	ds_read_b128 v[28:31], v113 offset:96
	v_fma_mixlo_f16 v3, v58, v20, v3
	ds_write_b16 v146, v3 offset:34816
	v_mul_f32_e32 v3, v82, v16
	v_fma_mixlo_f16 v3, v42, v20, v3
	v_cndmask_b32_e64 v59, v75, v59, s[2:3]
	ds_write_b16 v146, v3 offset:34880
	v_mul_f32_e32 v3, v13, v17
	v_fma_mixlo_f16 v3, v59, v21, v3
	v_cndmask_b32_e64 v43, v43, v27, s[2:3]
	ds_write_b16 v146, v3 offset:34944
	v_mul_f32_e32 v3, v83, v17
	v_fma_mixlo_f16 v3, v43, v21, v3
	v_cndmask_b32_e64 v60, v76, v60, s[2:3]
	ds_write_b16 v146, v3 offset:35008
	v_mul_f32_e32 v3, v14, v18
	v_fma_mixlo_f16 v3, v60, v22, v3
	ds_write_b16 v146, v3 offset:35072
	v_mul_f32_e32 v3, v84, v18
	ds_read_b128 v[24:27], v113 offset:224
	v_fma_mixlo_f16 v3, v44, v22, v3
	v_cndmask_b32_e64 v61, v77, v61, s[2:3]
	ds_write_b16 v146, v3 offset:35136
	v_mul_f32_e32 v3, v15, v19
	v_fma_mixlo_f16 v3, v61, v23, v3
	ds_write_b16 v146, v3 offset:35200
	v_mul_f32_e32 v3, v85, v19
	v_fma_mixlo_f16 v3, v45, v23, v3
	v_cndmask_b32_e64 v62, v78, v62, s[2:3]
	ds_write_b16 v146, v3 offset:35264
	s_waitcnt lgkmcnt(0)
	v_mul_f32_e32 v3, v4, v24
	v_fma_mixlo_f16 v3, v62, v28, v3
	ds_write_b16 v146, v3 offset:35840
	v_mul_f32_e32 v3, v8, v24
	v_fma_mixlo_f16 v3, v46, v28, v3
	v_cndmask_b32_e64 v63, v79, v63, s[2:3]
	ds_write_b16 v146, v3 offset:35904
	v_mul_f32_e32 v3, v5, v25
	v_fma_mixlo_f16 v3, v63, v29, v3
	ds_write_b16 v146, v3 offset:35968
	v_mul_f32_e32 v3, v9, v25
	v_fma_mixlo_f16 v3, v47, v29, v3
	v_cndmask_b32_e64 v64, v80, v64, s[2:3]
	ds_write_b16 v146, v3 offset:36032
	v_mul_f32_e32 v3, v6, v26
	v_fma_mixlo_f16 v3, v64, v30, v3
	v_cndmask_b32_e64 v32, v48, v32, s[2:3]
	ds_write_b16 v146, v3 offset:36096
	v_mul_f32_e32 v3, v10, v26
	v_fma_mixlo_f16 v3, v32, v30, v3
	v_cndmask_b32_e64 v65, v81, v65, s[2:3]
	ds_write_b16 v146, v3 offset:36160
	v_mul_f32_e32 v3, v7, v27
	v_fma_mixlo_f16 v3, v65, v31, v3
	v_cndmask_b32_e64 v33, v49, v33, s[2:3]
	ds_write_b16 v146, v3 offset:36224
	v_mul_f32_e32 v3, v11, v27
	v_fma_mixlo_f16 v3, v33, v31, v3
	s_or_b32 s1, s89, s1
	ds_write_b16 v146, v3 offset:36288
	v_ashrrev_i32_e32 v3, 2, v165
	s_and_b64 s[2:3], s[2:3], exec
	v_lshlrev_b32_e32 v4, 4, v165
	s_cselect_b32 s2, 0, 64
	v_readlane_b32 s3, v248, 5
	v_add_u32_e32 v8, s1, v3
	v_and_b32_e32 v14, 48, v4
	s_or_b32 s2, s2, s3
	v_lshlrev_b32_e32 v4, 7, v3
	v_lshlrev_b32_e32 v9, 6, v8
	v_lshlrev_b32_e32 v8, 2, v8
	s_waitcnt lgkmcnt(0)
	v_add3_u32 v10, s0, v4, v14
	v_and_b32_e32 v15, 0xffffffc0, v8
	s_ashr_i32 s2, s2, 5
	ds_read_b128 v[4:7], v10 offset:32768
	v_and_b32_e32 v9, 0x3c0, v9
	v_and_b32_e32 v11, 32, v8
	v_add_u32_e32 v8, s2, v15
	v_bitop3_b32 v150, v9, v11, v14 bitop3:0x36
	v_ashrrev_i32_e32 v9, 31, v8
	v_lshlrev_b64 v[8:9], 10, v[8:9]
	v_lshl_add_u64 v[8:9], s[66:67], 0, v[8:9]
	v_lshl_add_u64 v[12:13], v[8:9], 0, v[150:151]
	s_or_b32 s3, s2, 1
	ds_read_b128 v[8:11], v10 offset:32832
	s_waitcnt lgkmcnt(0)
	global_store_dwordx4 v[12:13], v[4:7], off sc1
	v_add_u32_e32 v3, 16, v3
	s_mov_b64 s[62:63], 0
	v_add_u32_e32 v4, s3, v15
	v_ashrrev_i32_e32 v5, 31, v4
	v_lshlrev_b64 v[4:5], 10, v[4:5]
	v_lshl_add_u64 v[4:5], s[66:67], 0, v[4:5]
	v_lshl_add_u64 v[4:5], v[4:5], 0, v[150:151]
	global_store_dwordx4 v[4:5], v[8:11], off sc1
	v_lshlrev_b32_e32 v4, 7, v3
	v_add_u32_e32 v3, s1, v3
	v_lshlrev_b32_e32 v8, 6, v3
	v_lshlrev_b32_e32 v3, 2, v3
	v_add3_u32 v10, s0, v4, v14
	v_and_b32_e32 v8, 0x3c0, v8
	v_and_b32_e32 v9, 32, v3
	v_and_b32_e32 v3, 0xffffffc0, v3
	ds_read_b128 v[4:7], v10 offset:32768
	v_bitop3_b32 v150, v8, v9, v14 bitop3:0x36
	v_add_u32_e32 v8, s2, v3
	v_ashrrev_i32_e32 v9, 31, v8
	v_lshlrev_b64 v[8:9], 10, v[8:9]
	v_lshl_add_u64 v[8:9], s[66:67], 0, v[8:9]
	v_lshl_add_u64 v[12:13], v[8:9], 0, v[150:151]
	ds_read_b128 v[8:11], v10 offset:32832
	s_waitcnt lgkmcnt(0)
	global_store_dwordx4 v[12:13], v[4:7], off sc1
	s_and_b64 vcc, exec, s[80:81]
	s_nop 0
	v_add_u32_e32 v4, s3, v3
	v_ashrrev_i32_e32 v5, 31, v4
	v_lshlrev_b64 v[4:5], 10, v[4:5]
	v_lshl_add_u64 v[4:5], s[66:67], 0, v[4:5]
	v_lshl_add_u64 v[4:5], v[4:5], 0, v[150:151]
	global_store_dwordx4 v[4:5], v[8:11], off sc1
	s_cbranch_vccnz .LBB1_44
.LBB1_2:
	v_mov_b32_e32 v55, v0
	s_xor_b64 s[80:81], s[62:63], -1
	v_readfirstlane_b32 s95, v55
	v_and_b32_e32 v165, 63, v55
	s_and_b32 s0, s95, 0x1fffffc0
	v_or_b32_e32 v3, s0, v165
	s_movk_i32 s0, 0x100
	v_cmp_gt_u32_e32 vcc, s0, v55
	v_lshlrev_b32_e32 v152, 3, v3
	s_ashr_i32 s33, s95, 6
	v_cndmask_b32_e32 v3, v158, v159, vcc
	v_add_u32_e32 v56, 0, v3
	v_lshlrev_b32_e32 v3, 3, v55
	v_lshlrev_b32_e32 v4, 4, v55
	v_lshrrev_b32_sdwa v5, v160, v55 dst_sel:DWORD dst_unused:UNUSED_PAD src0_sel:DWORD src1_sel:BYTE_0
	v_lshlrev_b32_sdwa v6, v161, v55 dst_sel:DWORD dst_unused:UNUSED_PAD src0_sel:DWORD src1_sel:BYTE_0
	s_and_b32 s88, s33, 3
	s_and_b64 vcc, exec, s[80:81]
	v_ashrrev_i32_e32 v153, 31, v152
	v_and_b32_e32 v150, 0x3f0, v4
	v_and_b32_e32 v52, 0xf0, v4
	v_mul_u32_u24_e32 v58, 0x104, v5
	v_and_b32_e32 v57, 56, v3
	v_and_b32_e32 v3, 0x3c0, v6
	v_and_b32_e32 v54, 48, v4
	v_mov_b32_e32 v60, 0
	v_mov_b32_e32 v59, 0
	s_cbranch_vccnz .LBB1_4
	v_ashrrev_i32_e32 v30, 8, v55
	v_readlane_b32 s0, v248, 15
	v_readlane_b32 s4, v248, 0
	v_mov_b32_e32 v23, v151
	v_add_u32_e32 v6, s0, v30
	v_and_b32_e32 v7, 31, v6
	v_lshlrev_b32_e32 v6, 1, v6
	v_and_b32_e32 v31, 0xffffffc0, v6
	v_lshlrev_b32_e32 v22, 8, v7
	v_readlane_b32 s5, v248, 1
	v_or_b32_e32 v18, v31, v5
	v_mov_b32_e32 v53, v151
	v_lshl_add_u64 v[6:7], s[4:5], 0, v[22:23]
	v_lshl_add_u64 v[20:21], v[6:7], 0, v[52:53]
	v_or_b32_e32 v6, 16, v18
	v_ashrrev_i32_e32 v7, 31, v6
	v_lshlrev_b64 v[6:7], 13, v[6:7]
	v_or_b32_e32 v10, 32, v18
	v_ashrrev_i32_e32 v19, 31, v18
	v_lshl_add_u64 v[6:7], v[20:21], 0, v[6:7]
	v_ashrrev_i32_e32 v11, 31, v10
	global_load_dwordx4 v[6:9], v[6:7], off nt
	v_lshlrev_b64 v[14:15], 13, v[18:19]
	v_lshlrev_b64 v[10:11], 13, v[10:11]
	v_or_b32_e32 v18, 48, v18
	v_lshl_add_u64 v[10:11], v[20:21], 0, v[10:11]
	v_ashrrev_i32_e32 v19, 31, v18
	global_load_dwordx4 v[10:13], v[10:11], off nt
	v_lshlrev_b64 v[18:19], 13, v[18:19]
	v_lshl_add_u64 v[14:15], v[20:21], 0, v[14:15]
	v_lshl_add_u64 v[18:19], v[20:21], 0, v[18:19]
	global_load_dwordx4 v[14:17], v[14:15], off nt
	s_lshl_b32 s0, s33, 10
	global_load_dwordx4 v[18:21], v[18:19], off nt
	v_lshlrev_b64 v[24:25], 1, v[152:153]
	s_add_i32 s2, s0, 0
	v_lshl_add_u64 v[26:27], s[74:75], 0, v[24:25]
	s_add_i32 m0, s2, 0x10000
	s_mov_b64 s[8:9], 0x2000
	global_load_lds_dwordx4 v[26:27], off
	v_lshl_add_u64 v[28:29], v[26:27], 0, s[8:9]
	s_add_i32 m0, s2, 0x12000
	s_mov_b64 s[10:11], 0x4000
	global_load_lds_dwordx4 v[28:29], off
	v_lshl_add_u64 v[28:29], v[26:27], 0, s[10:11]
	s_add_i32 m0, s2, 0x14000
	s_mov_b64 s[12:13], 0x6000
	v_readlane_b32 s0, v248, 6
	global_load_lds_dwordx4 v[28:29], off
	v_lshl_add_u64 v[26:27], v[26:27], 0, s[12:13]
	s_add_i32 m0, s2, 0x16000
	v_readlane_b32 s1, v248, 7
	global_load_lds_dwordx4 v[26:27], off
	s_nop 0
	v_lshl_add_u64 v[26:27], s[0:1], 0, v[24:25]
	v_readlane_b32 s0, v248, 8
	s_add_i32 m0, s2, 0x18000
	v_readlane_b32 s1, v248, 9
	global_load_lds_dwordx4 v[26:27], off
	s_nop 0
	v_lshl_add_u64 v[26:27], s[0:1], 0, v[24:25]
	v_readlane_b32 s0, v248, 10
	s_add_i32 m0, s2, 0x1a000
	v_readlane_b32 s1, v248, 11
	global_load_lds_dwordx4 v[26:27], off
	s_nop 0
	v_lshl_add_u64 v[26:27], s[0:1], 0, v[24:25]
	v_readlane_b32 s0, v248, 12
	s_add_i32 m0, s2, 0x1c000
	v_readlane_b32 s1, v248, 13
	global_load_lds_dwordx4 v[26:27], off
	s_nop 0
	v_lshl_add_u64 v[26:27], s[0:1], 0, v[24:25]
	s_lshl_b32 s0, s88, 13
	v_readlane_b32 s1, v248, 20
	s_add_i32 m0, s2, 0x1e000
	s_or_b32 s0, s0, s1
	s_add_u32 s0, s68, s0
	global_load_lds_dwordx4 v[26:27], off
	s_addc_u32 s1, s71, 0
	v_lshl_add_u64 v[24:25], s[76:77], 0, v[24:25]
	s_mov_b32 m0, s2
	global_load_dwordx4 v[114:117], v150, s[0:1]
	global_load_dwordx4 v[118:121], v150, s[0:1] offset:1024
	global_load_dwordx4 v[122:125], v150, s[0:1] offset:2048
	global_load_dwordx4 v[126:129], v150, s[0:1] offset:3072
	v_lshl_add_u64 v[28:29], v[24:25], 0, s[8:9]
	global_load_lds_dwordx4 v[24:25], off
	s_add_i32 m0, s2, 0x2000
	v_add3_u32 v23, v56, v52, v58
	global_load_lds_dwordx4 v[28:29], off
	v_lshl_add_u64 v[28:29], v[24:25], 0, s[10:11]
	s_add_i32 m0, s2, 0x4000
	v_lshl_add_u64 v[24:25], v[24:25], 0, s[12:13]
	global_load_lds_dwordx4 v[28:29], off
	s_add_i32 m0, s2, 0x6000
	v_lshl_add_u64 v[26:27], s[0:1], 0, v[150:151]
	s_movk_i32 s0, 0x1000
	global_load_lds_dwordx4 v[24:25], off
	v_add_u32_e32 v24, 0x1040, v23
	v_add_co_u32_e32 v26, vcc, s0, v26
	s_waitcnt vmcnt(0)
	ds_write2_b32 v24, v6, v7 offset1:1
	v_add_u32_e32 v6, 0x1048, v23
	v_addc_co_u32_e32 v27, vcc, 0, v27, vcc
	ds_write2_b32 v6, v8, v9 offset1:1
	v_add_u32_e32 v6, 0x2080, v23
	global_load_dwordx4 v[130:133], v[26:27], off
	global_load_dwordx4 v[134:137], v[26:27], off offset:1024
	ds_write2_b32 v6, v10, v11 offset1:1
	v_add_u32_e32 v6, 0x2088, v23
	ds_write2_b32 v6, v12, v13 offset1:1
	v_add_u32_e32 v6, 0x30c0, v23
	global_load_dwordx4 v[138:141], v[26:27], off offset:2048
	global_load_dwordx4 v[142:145], v[26:27], off offset:3072
	ds_write2_b32 v23, v14, v15 offset1:1
	ds_write2_b32 v23, v16, v17 offset0:2 offset1:3
	ds_write2_b32 v6, v18, v19 offset1:1
	v_add_u32_e32 v6, 0x30c8, v23
	ds_write2_b32 v6, v20, v21 offset1:1
	v_or_b32_e32 v6, v31, v57
	v_lshrrev_b32_sdwa v23, v162, v55 dst_sel:DWORD dst_unused:UNUSED_PAD src0_sel:DWORD src1_sel:BYTE_0
	v_ashrrev_i32_e32 v12, 5, v6
	v_mul_u32_u24_e32 v6, 0x41, v57
	v_and_b32_e32 v7, 0x7c, v23
	v_lshlrev_b32_e32 v6, 2, v6
	v_add3_u32 v16, v56, v7, v6
	s_waitcnt lgkmcnt(0)
	s_barrier
	v_add3_u32 v10, v56, v6, v7
	ds_read2_b32 v[6:7], v16 offset1:65
	ds_read2_b32 v[8:9], v16 offset0:130 offset1:195
	v_add_u32_e32 v20, 0x400, v10
	ds_read2_b32 v[10:11], v20 offset0:4 offset1:69
	v_add_u32_e32 v22, v12, v22
	ds_read2_b32 v[12:13], v20 offset0:134 offset1:199
	s_waitcnt lgkmcnt(3)
	v_cvt_pk_f16_f32 v6, v6, v7
	s_waitcnt lgkmcnt(2)
	v_cvt_pk_f16_f32 v7, v8, v9
	v_and_b32_e32 v9, 32, v23
	s_waitcnt lgkmcnt(1)
	v_cvt_pk_f16_f32 v8, v10, v11
	v_bitop3_b32 v10, v54, v9, v3 bitop3:0x36
	s_waitcnt lgkmcnt(0)
	v_cvt_pk_f16_f32 v9, v12, v13
	v_and_b32_e32 v12, 64, v23
	v_add_u32_e32 v12, v22, v12
	v_readlane_b32 s6, v248, 2
	v_readlane_b32 s7, v248, 3
	v_mov_b32_e32 v11, v151
	v_ashrrev_i32_e32 v13, 31, v12
	v_lshl_add_u64 v[10:11], s[6:7], 0, v[10:11]
	v_lshlrev_b64 v[12:13], 10, v[12:13]
	v_lshl_add_u64 v[12:13], v[10:11], 0, v[12:13]
	s_movk_i32 s0, 0xc0
	ds_read2_b32 v[14:15], v16 offset0:32 offset1:97
	ds_read2_b32 v[16:17], v16 offset0:162 offset1:227
	ds_read2_b32 v[18:19], v20 offset0:36 offset1:101
	ds_read2_b32 v[20:21], v20 offset0:166 offset1:231
	global_store_dwordx4 v[12:13], v[6:9], off sc1
	v_bitop3_b32 v12, v23, s0, v163 bitop3:0xc8
	v_add_u32_e32 v12, v22, v12
	v_ashrrev_i32_e32 v13, 31, v12
	v_lshlrev_b64 v[12:13], 10, v[12:13]
	s_waitcnt lgkmcnt(3)
	v_cvt_pk_f16_f32 v6, v14, v15
	s_waitcnt lgkmcnt(2)
	v_cvt_pk_f16_f32 v7, v16, v17
	v_lshl_add_u64 v[10:11], v[10:11], 0, v[12:13]
	v_readlane_b32 s0, v248, 16
	s_waitcnt lgkmcnt(1)
	v_cvt_pk_f16_f32 v8, v18, v19
	s_waitcnt lgkmcnt(0)
	v_cvt_pk_f16_f32 v9, v20, v21
	global_store_dwordx4 v[10:11], v[6:9], off sc1
	s_barrier
	s_nop 0
	v_add_u32_e32 v7, s0, v30
	v_lshlrev_b32_e32 v6, 1, v7
	v_and_b32_e32 v60, 0xffffffc0, v6
	v_or_b32_e32 v6, v60, v5
	v_lshlrev_b32_e32 v5, 6, v7
	v_and_b32_e32 v59, 0x7c0, v5
	v_lshlrev_b32_e32 v8, 2, v59
	v_mov_b32_e32 v9, v151
	v_ashrrev_i32_e32 v7, 31, v6
	v_lshl_add_u64 v[8:9], s[4:5], 0, v[8:9]
	v_lshlrev_b64 v[10:11], 13, v[6:7]
	v_or_b32_e32 v12, 16, v6
	v_or_b32_e32 v14, 32, v6
	v_or_b32_e32 v6, 48, v6
	v_lshl_add_u64 v[8:9], v[8:9], 0, v[52:53]
	v_ashrrev_i32_e32 v13, 31, v12
	v_ashrrev_i32_e32 v15, 31, v14
	v_ashrrev_i32_e32 v7, 31, v6
	v_lshl_add_u64 v[10:11], v[8:9], 0, v[10:11]
	v_lshlrev_b64 v[12:13], 13, v[12:13]
	v_lshlrev_b64 v[14:15], 13, v[14:15]
	v_lshlrev_b64 v[6:7], 13, v[6:7]
	v_lshl_add_u64 v[12:13], v[8:9], 0, v[12:13]
	v_lshl_add_u64 v[14:15], v[8:9], 0, v[14:15]
	v_lshl_add_u64 v[6:7], v[8:9], 0, v[6:7]
	global_load_dwordx4 v[36:39], v[10:11], off nt
	global_load_dwordx4 v[40:43], v[12:13], off nt
	global_load_dwordx4 v[44:47], v[14:15], off nt
	global_load_dwordx4 v[48:51], v[6:7], off nt

.LBB1_6:
	v_fmac_f32 v21, 0x3f800000, v1
	s_nop 8
	v_max_f32_e32 v62, v20, v20
	v_max_f32_e32 v61, v21, v21
	v_max_f32_e32 v61, v62, v61
	v_fmac_f32 v22, 0x40000000, v1
	v_fmac_f32 v23, 0x40400000, v1
	v_fmac_f32 v24, 0x41000000, v1
	v_fmac_f32 v25, 0x41100000, v1
	v_fmac_f32 v26, 0x41200000, v1
	v_fmac_f32 v27, 0x41300000, v1
	v_fmac_f32 v28, 0x41800000, v1
	s_nop 0
	v_max3_f32 v61, v61, v22, v23
	v_max3_f32 v61, v61, v24, v25
	v_max3_f32 v61, v61, v26, v27
	v_fmac_f32 v29, 0x41880000, v1
	v_fmac_f32 v30, 0x41900000, v1
	v_fmac_f32 v31, 0x41980000, v1
	v_fmac_f32 v32, 0x41c00000, v1
	v_fmac_f32 v33, 0x41c80000, v1
	v_fmac_f32 v34, 0x41d00000, v1
	s_nop 0
	v_max3_f32 v61, v61, v28, v29
	v_max3_f32 v61, v61, v30, v31
	v_max3_f32 v61, v61, v32, v33
	v_fmac_f32 v35, 0x41d80000, v1
	v_fmac_f32 v4, 0x42000000, v1
	v_fmac_f32 v5, 0x42040000, v1
	v_fmac_f32 v6, 0x42080000, v1
	v_fmac_f32 v7, 0x420c0000, v1
	v_fmac_f32 v8, 0x42200000, v1
	s_nop 0
	v_max3_f32 v61, v61, v34, v35
	v_max3_f32 v61, v61, v4, v5
	v_max3_f32 v61, v61, v6, v7
	v_fmac_f32 v9, 0x42240000, v1
	v_fmac_f32 v10, 0x42280000, v1
	v_fmac_f32 v11, 0x422c0000, v1
	v_cvt_f32_i32_e32 v53, v53
	v_max3_f32 v61, v61, v8, v9
	v_max3_f32 v61, v61, v10, v11
	v_fmac_f32 v12, 0x42400000, v1
	v_fmac_f32 v13, 0x42440000, v1
	v_fmac_f32 v14, 0x42480000, v1
	v_fmac_f32 v15, 0x424c0000, v1
	v_fmac_f32 v16, 0x42600000, v1
	v_fmac_f32 v17, 0x42640000, v1
	v_fmac_f32 v18, 0x42680000, v1
	s_nop 0
	v_max3_f32 v61, v61, v12, v13
	v_max3_f32 v61, v61, v14, v15
	v_max3_f32 v61, v61, v16, v17
	v_fmac_f32 v19, 0x426c0000, v1
	v_cndmask_b32_e64 v63, 0, 1, s[62:63]
	v_max3_f32 v61, v61, v18, v19
	v_fma_f32 v61, -v1, v53, v61
	v_mov_b32_e32 v62, v61
	v_cmp_ne_u32_e64 s[0:1], 1, v63
	s_andn2_b64 vcc, exec, s[62:63]
	v_permlane32_swap_b32_e32 v61, v62
	s_cbranch_vccnz .LBB1_8
	v_add3_u32 v52, v56, v52, v58
	s_waitcnt vmcnt(3)
	ds_write2_b32 v52, v36, v37 offset1:1
	ds_write2_b32 v52, v38, v39 offset0:2 offset1:3
	v_add_u32_e32 v36, 0x1040, v52
	s_waitcnt vmcnt(2)
	ds_write2_b32 v36, v40, v41 offset1:1
	v_add_u32_e32 v36, 0x1048, v52
	ds_write2_b32 v36, v42, v43 offset1:1
	v_add_u32_e32 v36, 0x2080, v52
	s_waitcnt vmcnt(1)
	ds_write2_b32 v36, v44, v45 offset1:1
	v_add_u32_e32 v36, 0x2088, v52
	ds_write2_b32 v36, v46, v47 offset1:1
	v_add_u32_e32 v36, 0x30c0, v52
	s_waitcnt vmcnt(0)
	ds_write2_b32 v36, v48, v49 offset1:1
	v_add_u32_e32 v36, 0x30c8, v52
	ds_write2_b32 v36, v50, v51 offset1:1
	v_lshrrev_b32_sdwa v44, v161, v55 dst_sel:DWORD dst_unused:UNUSED_PAD src0_sel:DWORD src1_sel:BYTE_0
	v_mul_u32_u24_e32 v36, 0x41, v57
	v_lshlrev_b32_e32 v46, 2, v44
	v_lshlrev_b32_e32 v36, 2, v36
	v_add3_u32 v47, v56, v46, v36
	v_add3_u32 v40, v56, v36, v46
	s_waitcnt lgkmcnt(0)
	s_barrier
	ds_read2_b32 v[36:37], v47 offset1:65
	ds_read2_b32 v[38:39], v47 offset0:130 offset1:195
	v_add_u32_e32 v50, 0x400, v40
	ds_read2_b32 v[40:41], v50 offset0:4 offset1:69
	ds_read2_b32 v[42:43], v50 offset0:134 offset1:199
	s_waitcnt lgkmcnt(3)
	v_cvt_pk_f16_f32 v36, v36, v37
	s_waitcnt lgkmcnt(2)
	v_cvt_pk_f16_f32 v37, v38, v39
	s_waitcnt lgkmcnt(1)
	v_cvt_pk_f16_f32 v38, v40, v41
	v_or_b32_e32 v41, v59, v44
	v_and_b32_e32 v40, 32, v46
	v_or_b32_e32 v45, v60, v57
	v_bitop3_b32 v40, v3, v40, v54 bitop3:0x36
	v_lshlrev_b32_e32 v3, 2, v41
	v_ashrrev_i32_e32 v52, 5, v45
	v_and_b32_e32 v41, 0x1f40, v3
	s_waitcnt lgkmcnt(0)
	v_cvt_pk_f16_f32 v39, v42, v43
	v_add_u32_e32 v42, v41, v52
	v_ashrrev_i32_e32 v43, 31, v42
	v_readlane_b32 s4, v248, 0
	v_lshlrev_b64 v[42:43], 10, v[42:43]
	v_readlane_b32 s6, v248, 2
	v_readlane_b32 s7, v248, 3
	v_mov_b32_e32 v41, v151
	s_movk_i32 s2, 0x1fc0
	v_lshl_add_u64 v[42:43], s[6:7], 0, v[42:43]
	v_lshl_add_u64 v[42:43], v[42:43], 0, v[40:41]
	v_bitop3_b32 v3, v3, s2, v163 bitop3:0xc8
	ds_read2_b32 v[44:45], v47 offset0:32 offset1:97
	ds_read2_b32 v[46:47], v47 offset0:162 offset1:227
	ds_read2_b32 v[48:49], v50 offset0:36 offset1:101
	ds_read2_b32 v[50:51], v50 offset0:166 offset1:231
	global_store_dwordx4 v[42:43], v[36:39], off sc1
	v_add_u32_e32 v42, v3, v52
	v_ashrrev_i32_e32 v43, 31, v42
	v_lshlrev_b64 v[42:43], 10, v[42:43]
	v_lshl_add_u64 v[42:43], s[6:7], 0, v[42:43]
	v_lshl_add_u64 v[40:41], v[42:43], 0, v[40:41]
	v_readlane_b32 s5, v248, 1
	s_waitcnt lgkmcnt(3)
	v_cvt_pk_f16_f32 v36, v44, v45
	s_waitcnt lgkmcnt(2)
	v_cvt_pk_f16_f32 v37, v46, v47
	s_waitcnt lgkmcnt(1)
	v_cvt_pk_f16_f32 v38, v48, v49
	s_waitcnt lgkmcnt(0)
	v_cvt_pk_f16_f32 v39, v50, v51
	global_store_dwordx4 v[40:41], v[36:39], off sc1
.LBB1_8:
	s_mov_b32 s2, 0xf149f2ca
	v_max3_f32 v178, v61, v62, s2
	v_fma_f32 v3, -v1, v53, -v178
	s_waitcnt vmcnt(3)
	v_mul_f32_e32 v36, 0x3e0293ee, v3
	v_fmamk_f32 v3, v20, 0x3e0293ee, v36
	s_lshl_b32 s2, s33, 9
	v_exp_f32_e32 v190, v3
	v_sub_f32_e32 v3, 0xf149f2ca, v178
	s_add_i32 s92, s2, 0
	v_fmamk_f32 v20, v21, 0x3e0293ee, v36
	v_fmamk_f32 v21, v22, 0x3e0293ee, v36
	v_fmamk_f32 v22, v23, 0x3e0293ee, v36
	v_fmamk_f32 v23, v24, 0x3e0293ee, v36
	v_fmamk_f32 v24, v25, 0x3e0293ee, v36
	v_fmamk_f32 v25, v26, 0x3e0293ee, v36
	v_fmamk_f32 v26, v27, 0x3e0293ee, v36
	v_fmamk_f32 v27, v28, 0x3e0293ee, v36
	v_fmamk_f32 v28, v29, 0x3e0293ee, v36
	v_fmamk_f32 v29, v30, 0x3e0293ee, v36
	v_fmamk_f32 v30, v31, 0x3e0293ee, v36
	v_fmamk_f32 v31, v32, 0x3e0293ee, v36
	v_fmamk_f32 v32, v33, 0x3e0293ee, v36
	v_fmamk_f32 v33, v34, 0x3e0293ee, v36
	v_fmamk_f32 v34, v35, 0x3e0293ee, v36
	v_mul_f32_e32 v3, 0x3e0293ee, v3
	v_pk_fma_f32 v[98:99], v[4:5], s[94:95], v[36:37] op_sel_hi:[1,0,0]
	s_add_i32 s92, s92, 0x20000
	v_lshlrev_b32_e32 v4, 4, v165
	v_exp_f32_e32 v191, v20
	v_exp_f32_e32 v188, v21
	v_exp_f32_e32 v189, v22
	v_exp_f32_e32 v186, v23
	v_exp_f32_e32 v187, v24
	v_exp_f32_e32 v184, v25
	v_exp_f32_e32 v185, v26
	v_exp_f32_e32 v182, v27
	v_exp_f32_e32 v183, v28
	v_exp_f32_e32 v156, v29
	v_exp_f32_e32 v157, v30
	v_exp_f32_e32 v148, v31
	v_exp_f32_e32 v149, v32
	v_exp_f32_e32 v146, v33
	v_exp_f32_e32 v147, v34
	v_exp_f32_e32 v170, v3
	s_cmp_lg_u32 0, -1
	v_lshlrev_b32_e32 v3, 3, v165
	v_and_b32_e32 v4, 0xc0, v4
	v_lshlrev_b32_e32 v5, 1, v165
	v_pk_fma_f32 v[100:101], v[6:7], s[94:95], v[36:37] op_sel_hi:[1,0,0]
	s_cselect_b32 s2, 0, 0
	v_and_or_b32 v4, v3, 24, v4
	v_and_b32_e32 v5, 32, v5
	v_and_b32_e32 v6, 0x100, v3
	s_add_i32 s64, s64, s2
	v_or3_b32 v4, v4, v5, v6
	v_pk_fma_f32 v[112:113], v[18:19], s[94:95], v[36:37] op_sel_hi:[1,0,0]
	v_pk_fma_f32 v[110:111], v[16:17], s[94:95], v[36:37] op_sel_hi:[1,0,0]
	v_pk_fma_f32 v[108:109], v[14:15], s[94:95], v[36:37] op_sel_hi:[1,0,0]
	v_pk_fma_f32 v[106:107], v[12:13], s[94:95], v[36:37] op_sel_hi:[1,0,0]
	v_pk_fma_f32 v[104:105], v[10:11], s[94:95], v[36:37] op_sel_hi:[1,0,0]
	v_pk_fma_f32 v[102:103], v[8:9], s[94:95], v[36:37] op_sel_hi:[1,0,0]
	s_mov_b32 s72, 1
	v_add_u32_e32 v169, s64, v4
	s_cmp_lt_u32 s83, 2
	s_barrier
	s_cbranch_scc1 .LBB1_25
	s_lshl_b32 s5, s95, 3
	s_and_b32 s5, s5, 0xfffffe00
	v_or_b32_e32 v4, s5, v3
	s_add_i32 s5, s90, s89
	s_addk_i32 s5, 0xff00
	v_add_u32_e32 v3, s5, v167
	v_ashrrev_i32_e32 v5, 31, v4
	v_sub_u32_e32 v3, v3, v168
	v_mov_b32_e32 v16, v2
	v_mov_b32_e32 v17, v2
	s_lshl_b32 s4, s33, 10
	v_lshlrev_b64 v[154:155], 1, v[4:5]
	v_add_u32_e32 v250, 0x2000, v154
	v_add_u32_e32 v251, 0x4000, v154
	v_add_u32_e32 v252, 0x6000, v154
	v_subrev_u32_e32 v179, s82, v3
	v_mov_b32_e32 v3, v2
	v_mov_b32_e32 v4, v2
	v_mov_b32_e32 v5, v2
	v_mov_b32_e32 v6, v2
	v_mov_b32_e32 v7, v2
	v_mov_b32_e32 v8, v2
	v_mov_b32_e32 v9, v2
	v_mov_b32_e32 v10, v2
	v_mov_b32_e32 v11, v2
	v_mov_b32_e32 v12, v2
	v_mov_b32_e32 v13, v2
	v_mov_b32_e32 v14, v2
	v_mov_b32_e32 v15, v2
	s_waitcnt vmcnt(0)
	v_mov_b64_e32 v[48:49], v[16:17]
	v_mov_b64_e32 v[80:81], v[16:17]
	v_mov_b64_e32 v[32:33], v[16:17]
	v_mov_b64_e32 v[64:65], v[16:17]
	s_mov_b32 s70, s68
	v_cmp_gt_u32_e64 s[2:3], 32, v165
	v_lshl_add_u32 v176, v167, 2, s92
	v_lshl_add_u32 v177, v168, 2, s92
	s_add_i32 s68, s82, 0x13f
	v_mov_b32_e32 v166, 0
	s_add_i32 s69, s4, 0
	s_mov_b64 s[84:85], s[76:77]
	v_mov_b64_e32 v[46:47], v[14:15]
	v_mov_b64_e32 v[44:45], v[12:13]
	v_mov_b64_e32 v[42:43], v[10:11]
	v_mov_b64_e32 v[40:41], v[8:9]
	v_mov_b64_e32 v[38:39], v[6:7]
	v_mov_b64_e32 v[36:37], v[4:5]
	v_mov_b64_e32 v[34:35], v[2:3]
	v_mov_b64_e32 v[78:79], v[14:15]
	v_mov_b64_e32 v[76:77], v[12:13]
	v_mov_b64_e32 v[74:75], v[10:11]
	v_mov_b64_e32 v[72:73], v[8:9]
	v_mov_b64_e32 v[70:71], v[6:7]
	v_mov_b64_e32 v[68:69], v[4:5]
	v_mov_b64_e32 v[66:67], v[2:3]
	v_mov_b64_e32 v[30:31], v[14:15]
	v_mov_b64_e32 v[28:29], v[12:13]
	v_mov_b64_e32 v[26:27], v[10:11]
	v_mov_b64_e32 v[24:25], v[8:9]
	v_mov_b64_e32 v[22:23], v[6:7]
	v_mov_b64_e32 v[20:21], v[4:5]
	v_mov_b64_e32 v[18:19], v[2:3]
	v_mov_b64_e32 v[62:63], v[14:15]
	v_mov_b64_e32 v[60:61], v[12:13]
	v_mov_b64_e32 v[58:59], v[10:11]
	v_mov_b64_e32 v[56:57], v[8:9]
	v_mov_b64_e32 v[54:55], v[6:7]
	v_mov_b64_e32 v[52:53], v[4:5]
	v_mov_b64_e32 v[50:51], v[2:3]
	s_branch .LBB1_12

.LBB1_12:
	ds_read_b128 v[4:7], v172 offset:32768
	ds_read_b128 v[8:11], v172 offset:32896
	ds_read_b128 v[192:195], v172 offset:40960
	ds_read_b128 v[196:199], v172 offset:41088
	ds_read_b128 v[12:15], v173 offset:32768
	ds_read_b128 v[200:203], v173 offset:32896
	ds_read_b128 v[204:207], v173 offset:40960
	ds_read_b128 v[208:211], v173 offset:41088
	s_waitcnt lgkmcnt(7)
	v_mfma_f32_32x32x16_f16 v[82:97], v[4:7], v[114:117], 0
	ds_read_b128 v[4:7], v174 offset:32768
	ds_read_b128 v[212:215], v174 offset:32896
	ds_read_b128 v[216:219], v174 offset:40960
	ds_read_b128 v[220:223], v174 offset:41088
	ds_read_b128 v[224:227], v175 offset:32768
	ds_read_b128 v[228:231], v175 offset:32896
	ds_read_b128 v[232:235], v175 offset:40960
	ds_read_b128 v[236:239], v175 offset:41088
	v_add_f32_e32 v3, 0, v190
	v_add_f32_e32 v3, v191, v3
	v_add_f32_e32 v3, v188, v3
	v_add_f32_e32 v3, v189, v3
	v_add_f32_e32 v3, v186, v3
	v_add_f32_e32 v3, v187, v3
	s_waitcnt lgkmcnt(11)
	v_mfma_f32_32x32x16_f16 v[82:97], v[12:15], v[118:121], v[82:97]
	v_add_f32_e32 v3, v184, v3
	v_add_f32_e32 v3, v185, v3
	v_add_f32_e32 v3, v182, v3
	v_add_f32_e32 v3, v183, v3
	v_add_f32_e32 v3, v156, v3
	v_add_f32_e32 v3, v157, v3
	v_exp_f32_e32 v12, v98
	s_waitcnt lgkmcnt(7)
	v_mfma_f32_32x32x16_f16 v[82:97], v[4:7], v[122:125], v[82:97]
	v_add_f32_e32 v3, v148, v3
	v_exp_f32_e32 v13, v99
	v_add_f32_e32 v3, v149, v3
	v_exp_f32_e32 v14, v100
	v_add_f32_e32 v3, v146, v3
	v_exp_f32_e32 v15, v101
	v_add_f32_e32 v3, v147, v3
	s_waitcnt lgkmcnt(3)
	v_mfma_f32_32x32x16_f16 v[82:97], v[224:227], v[126:129], v[82:97]
	v_exp_f32_e32 v16, v102
	v_add_f32_e32 v3, v12, v3
	v_exp_f32_e32 v17, v103
	v_add_f32_e32 v3, v13, v3
	v_exp_f32_e32 v98, v104
	v_add_f32_e32 v3, v14, v3
	v_exp_f32_e32 v99, v105
	v_mfma_f32_32x32x16_f16 v[82:97], v[8:11], v[130:133], v[82:97]
	v_add_f32_e32 v3, v15, v3
	v_exp_f32_e32 v100, v106
	v_add_f32_e32 v3, v16, v3
	v_exp_f32_e32 v101, v107
	v_add_f32_e32 v3, v17, v3
	v_exp_f32_e32 v102, v108
	v_add_f32_e32 v3, v98, v3
	v_mfma_f32_32x32x16_f16 v[82:97], v[200:203], v[134:137], v[82:97]
	v_exp_f32_e32 v103, v109
	v_add_f32_e32 v3, v99, v3
	v_exp_f32_e32 v104, v110
	v_add_f32_e32 v3, v100, v3
	v_exp_f32_e32 v105, v111
	v_add_f32_e32 v3, v101, v3
	v_exp_f32_e32 v106, v112
	v_mfma_f32_32x32x16_f16 v[82:97], v[212:215], v[138:141], v[82:97]
	v_add_f32_e32 v3, v102, v3
	v_exp_f32_e32 v107, v113
	v_add_f32_e32 v3, v103, v3
	v_add_f32_e32 v3, v104, v3
	v_add_f32_e32 v3, v105, v3
	v_add_f32_e32 v3, v106, v3
	v_add_f32_e32 v3, v107, v3
	s_waitcnt lgkmcnt(2)
	v_mfma_f32_32x32x16_f16 v[82:97], v[228:231], v[142:145], v[82:97]
	v_mov_b32_e32 v180, v3
	v_cvt_pk_f16_f32 v4, v190, v191
	v_cvt_pk_f16_f32 v5, v188, v189
	v_cvt_pk_f16_f32 v6, v186, v187
	v_cvt_pk_f16_f32 v7, v184, v185
	v_cvt_pk_f16_f32 v8, v182, v183
	v_cvt_pk_f16_f32 v9, v156, v157
	v_cvt_pk_f16_f32 v10, v148, v149
	v_cvt_pk_f16_f32 v11, v146, v147
	v_cvt_pk_f16_f32 v12, v12, v13
	v_cvt_pk_f16_f32 v13, v14, v15
	v_cvt_pk_f16_f32 v14, v16, v17
	v_cvt_pk_f16_f32 v15, v98, v99
	v_cvt_pk_f16_f32 v146, v100, v101
	v_cvt_pk_f16_f32 v147, v102, v103
	v_cvt_pk_f16_f32 v148, v104, v105
	v_cvt_pk_f16_f32 v149, v106, v107
	s_nop 1
	v_permlane32_swap_b32_e32 v3, v180
	v_permlane32_swap_b32_e32 v4, v6
	v_permlane32_swap_b32_e32 v5, v7
	v_permlane32_swap_b32_e32 v8, v10
	v_permlane32_swap_b32_e32 v9, v11
	v_permlane32_swap_b32_e32 v12, v14
	v_permlane32_swap_b32_e32 v13, v15
	v_permlane32_swap_b32_e32 v146, v148
	v_permlane32_swap_b32_e32 v147, v149
	s_add_u32 s4, s74, 0x10000
	s_addc_u32 s5, s75, 0
	s_add_u32 s6, s76, 0x8000
	s_addc_u32 s7, s77, 0
	s_add_i32 m0, s69, 0x10000
	v_mfma_f32_32x32x16_f16 v[98:113], v[192:195], v[114:117], 0
	global_load_lds_dwordx4 v154, s[4:5]
	s_add_i32 m0, s69, 0x12000
	v_mfma_f32_32x32x16_f16 v[98:113], v[204:207], v[118:121], v[98:113]
	global_load_lds_dwordx4 v250, s[4:5]
	s_add_i32 m0, s69, 0x14000
	v_mfma_f32_32x32x16_f16 v[98:113], v[216:219], v[122:125], v[98:113]
	global_load_lds_dwordx4 v251, s[4:5]
	s_add_i32 m0, s69, 0x16000
	s_waitcnt lgkmcnt(0)
	v_mfma_f32_32x32x16_f16 v[98:113], v[232:235], v[126:129], v[98:113]
	global_load_lds_dwordx4 v252, s[4:5]
	s_add_i32 m0, s69, 0x8000
	v_mfma_f32_32x32x16_f16 v[98:113], v[196:199], v[130:133], v[98:113]
	global_load_lds_dwordx4 v154, s[6:7]
	s_add_i32 m0, s69, 0xa000
	v_mfma_f32_32x32x16_f16 v[98:113], v[208:211], v[134:137], v[98:113]
	global_load_lds_dwordx4 v250, s[6:7]
	s_add_i32 m0, s69, 0xc000
	v_mfma_f32_32x32x16_f16 v[98:113], v[220:223], v[138:141], v[98:113]
	global_load_lds_dwordx4 v251, s[6:7]
	s_add_i32 m0, s69, 0xe000
	v_mfma_f32_32x32x16_f16 v[98:113], v[236:239], v[142:145], v[98:113]
	global_load_lds_dwordx4 v252, s[6:7]
	s_add_i32 s4, s68, 0xffffff80
	s_cmp_le_i32 s4, s93
	v_add_u32_e32 v181, 0x80, v179
	s_cbranch_scc1 .LBB1_14
	v_cmp_gt_i32_e64 s[62:63], 26, v181
	v_cmp_gt_i32_e64 s[64:65], 27, v181
	v_cmp_gt_i32_e64 s[60:61], 25, v181
	s_and_b64 s[62:63], s[64:65], s[62:63]
	v_cmp_gt_i32_e64 s[58:59], 24, v181
	s_and_b64 s[60:61], s[62:63], s[60:61]
	v_cmp_gt_i32_e64 s[56:57], 19, v181
	s_and_b64 s[58:59], s[60:61], s[58:59]
	v_cmp_gt_i32_e64 s[54:55], 18, v181
	s_and_b64 s[56:57], s[58:59], s[56:57]
	v_cmp_gt_i32_e64 s[52:53], 17, v181
	s_and_b64 s[54:55], s[56:57], s[54:55]
	v_cmp_gt_i32_e64 s[50:51], 16, v181
	s_and_b64 s[52:53], s[54:55], s[52:53]
	v_cmp_gt_i32_e64 s[48:49], 11, v181
	s_and_b64 s[50:51], s[52:53], s[50:51]
	v_cmp_gt_i32_e64 s[46:47], 10, v181
	s_and_b64 s[48:49], s[50:51], s[48:49]
	v_cmp_gt_i32_e64 s[44:45], 9, v181
	s_and_b64 s[46:47], s[48:49], s[46:47]
	v_cmp_gt_i32_e64 s[42:43], 8, v181
	s_and_b64 s[44:45], s[46:47], s[44:45]
	v_cmp_gt_i32_e64 s[40:41], 3, v181
	s_and_b64 s[42:43], s[44:45], s[42:43]
	v_cmp_gt_i32_e64 s[38:39], 2, v181
	s_and_b64 s[40:41], s[42:43], s[40:41]
	v_cmp_gt_i32_e64 s[36:37], 1, v181
	s_and_b64 s[38:39], s[40:41], s[38:39]
	v_cmp_gt_i32_e64 s[34:35], 0, v181
	s_and_b64 s[36:37], s[38:39], s[36:37]
	s_and_b64 s[34:35], s[36:37], s[34:35]
	v_cmp_gt_i32_e64 s[30:31], 58, v181
	v_cndmask_b32_e64 v82, v82, v164, s[34:35]
	v_cmp_gt_i32_e64 s[34:35], 59, v181
	v_cmp_gt_i32_e64 s[28:29], 57, v181
	s_and_b64 s[30:31], s[34:35], s[30:31]
	v_cmp_gt_i32_e64 s[26:27], 56, v181
	s_and_b64 s[28:29], s[30:31], s[28:29]
	v_cmp_gt_i32_e64 s[24:25], 51, v181
	s_and_b64 s[26:27], s[28:29], s[26:27]
	v_cmp_gt_i32_e64 s[22:23], 50, v181
	s_and_b64 s[24:25], s[26:27], s[24:25]
	v_cmp_gt_i32_e64 s[20:21], 49, v181
	s_and_b64 s[22:23], s[24:25], s[22:23]
	v_cmp_gt_i32_e64 s[18:19], 48, v181
	s_and_b64 s[20:21], s[22:23], s[20:21]
	v_cmp_gt_i32_e64 s[16:17], 43, v181
	s_and_b64 s[18:19], s[20:21], s[18:19]
	v_cmp_gt_i32_e64 s[14:15], 42, v181
	s_and_b64 s[16:17], s[18:19], s[16:17]
	v_cmp_gt_i32_e64 s[12:13], 41, v181
	s_and_b64 s[14:15], s[16:17], s[14:15]
	v_cmp_gt_i32_e64 s[10:11], 40, v181
	s_and_b64 s[12:13], s[14:15], s[12:13]
	v_cmp_gt_i32_e64 s[8:9], 35, v181
	s_and_b64 s[10:11], s[12:13], s[10:11]
	v_cmp_gt_i32_e64 s[6:7], 34, v181
	s_and_b64 s[8:9], s[10:11], s[8:9]
	v_cmp_gt_i32_e64 s[4:5], 33, v181
	s_and_b64 s[6:7], s[8:9], s[6:7]
	v_cmp_gt_i32_e32 vcc, 32, v181
	s_and_b64 s[4:5], s[6:7], s[4:5]
	s_and_b64 vcc, s[4:5], vcc
	v_cndmask_b32_e64 v97, v97, v164, s[64:65]
	v_cndmask_b32_e64 v96, v96, v164, s[62:63]
	v_cndmask_b32_e64 v95, v95, v164, s[60:61]
	v_cndmask_b32_e64 v94, v94, v164, s[58:59]
	v_cndmask_b32_e64 v93, v93, v164, s[56:57]
	v_cndmask_b32_e64 v92, v92, v164, s[54:55]
	v_cndmask_b32_e64 v91, v91, v164, s[52:53]
	v_cndmask_b32_e64 v90, v90, v164, s[50:51]
	v_cndmask_b32_e64 v89, v89, v164, s[48:49]
	v_cndmask_b32_e64 v88, v88, v164, s[46:47]
	v_cndmask_b32_e64 v87, v87, v164, s[44:45]
	v_cndmask_b32_e64 v86, v86, v164, s[42:43]
	v_cndmask_b32_e64 v85, v85, v164, s[40:41]
	v_cndmask_b32_e64 v84, v84, v164, s[38:39]
	v_cndmask_b32_e64 v83, v83, v164, s[36:37]
	v_cndmask_b32_e64 v113, v113, v164, s[34:35]
	v_cndmask_b32_e64 v112, v112, v164, s[30:31]
	v_cndmask_b32_e64 v111, v111, v164, s[28:29]
	v_cndmask_b32_e64 v110, v110, v164, s[26:27]
	v_cndmask_b32_e64 v109, v109, v164, s[24:25]
	v_cndmask_b32_e64 v108, v108, v164, s[22:23]
	v_cndmask_b32_e64 v107, v107, v164, s[20:21]
	v_cndmask_b32_e64 v106, v106, v164, s[18:19]
	v_cndmask_b32_e64 v105, v105, v164, s[16:17]
	v_cndmask_b32_e64 v104, v104, v164, s[14:15]
	v_cndmask_b32_e64 v103, v103, v164, s[12:13]
	v_cndmask_b32_e64 v102, v102, v164, s[10:11]
	v_cndmask_b32_e64 v101, v101, v164, s[8:9]
	v_cndmask_b32_e64 v100, v100, v164, s[6:7]
	v_cndmask_b32_e64 v99, v99, v164, s[4:5]
	v_cndmask_b32_e32 v98, v98, v164, vcc

.LBB1_18:
	v_mul_f32_e64 v4, -v1, v183
	v_sub_f32_e32 v4, v4, v182
	v_mul_f32_e32 v178, 0x3e0293ee, v4
	v_fmamk_f32 v4, v82, 0x3e0293ee, v178
	v_fmamk_f32 v5, v83, 0x3e0293ee, v178
	v_fmamk_f32 v6, v84, 0x3e0293ee, v178
	v_fmamk_f32 v7, v85, 0x3e0293ee, v178
	v_fmamk_f32 v8, v86, 0x3e0293ee, v178
	v_fmamk_f32 v9, v87, 0x3e0293ee, v178
	v_fmamk_f32 v10, v88, 0x3e0293ee, v178
	v_fmamk_f32 v11, v89, 0x3e0293ee, v178
	v_fmamk_f32 v12, v90, 0x3e0293ee, v178
	v_fmamk_f32 v13, v91, 0x3e0293ee, v178
	v_fmamk_f32 v14, v92, 0x3e0293ee, v178
	v_fmamk_f32 v15, v93, 0x3e0293ee, v178
	v_fmamk_f32 v82, v94, 0x3e0293ee, v178
	v_fmamk_f32 v83, v95, 0x3e0293ee, v178
	v_fmamk_f32 v84, v96, 0x3e0293ee, v178
	v_fmamk_f32 v85, v97, 0x3e0293ee, v178
	v_fmamk_f32 v192, v99, 0x3e0293ee, v178
	v_fmamk_f32 v193, v100, 0x3e0293ee, v178
	v_fmamk_f32 v183, v98, 0x3e0293ee, v178
	v_fmamk_f32 v218, v101, 0x3e0293ee, v178
	v_fmamk_f32 v219, v102, 0x3e0293ee, v178
	v_fmamk_f32 v220, v103, 0x3e0293ee, v178
	v_fmamk_f32 v221, v104, 0x3e0293ee, v178
	v_fmamk_f32 v222, v105, 0x3e0293ee, v178
	v_fmamk_f32 v223, v106, 0x3e0293ee, v178
	v_fmamk_f32 v224, v107, 0x3e0293ee, v178
	v_fmamk_f32 v225, v108, 0x3e0293ee, v178
	v_fmamk_f32 v226, v109, 0x3e0293ee, v178
	v_fmamk_f32 v227, v110, 0x3e0293ee, v178
	v_fmamk_f32 v228, v111, 0x3e0293ee, v178
	v_fmamk_f32 v229, v112, 0x3e0293ee, v178
	v_fmac_f32_e32 v178, 0x3e0293ee, v113
	v_exp_f32_e32 v230, v4
	v_exp_f32_e32 v231, v5
	v_exp_f32_e32 v232, v6
	v_exp_f32_e32 v233, v7
	v_exp_f32_e32 v234, v8
	v_exp_f32_e32 v235, v9
	v_exp_f32_e32 v236, v10
	v_exp_f32_e32 v237, v11
	v_exp_f32_e32 v238, v12
	v_exp_f32_e32 v239, v13
	v_exp_f32_e32 v240, v14
	v_exp_f32_e32 v241, v15
	v_exp_f32_e32 v242, v82
	v_exp_f32_e32 v243, v83
	v_exp_f32_e32 v244, v84
	v_exp_f32_e32 v245, v85
	s_waitcnt vmcnt(0)
	s_barrier
	ds_read_b128 v[4:7], v172
	ds_read_b128 v[8:11], v172 offset:128
	v_exp_f32_e32 v183, v183
	v_exp_f32_e32 v246, v192
	v_exp_f32_e32 v247, v193
	s_waitcnt lgkmcnt(1)
	v_mfma_f32_32x32x16_f16 v[98:113], v[4:7], v[114:117], 0
	ds_read_b128 v[4:7], v172 offset:8192
	ds_read_b128 v[12:15], v172 offset:8320
	v_exp_f32_e32 v218, v218
	v_exp_f32_e32 v219, v219
	v_exp_f32_e32 v220, v220
	v_exp_f32_e32 v221, v221
	v_exp_f32_e32 v222, v222
	v_exp_f32_e32 v223, v223
	s_waitcnt lgkmcnt(1)
	v_mfma_f32_32x32x16_f16 v[82:97], v[4:7], v[114:117], 0
	ds_read_b128 v[4:7], v173
	ds_read_b128 v[146:149], v173 offset:8192
	ds_read_b128 v[184:187], v173 offset:128
	v_exp_f32_e32 v224, v224
	v_exp_f32_e32 v225, v225
	v_exp_f32_e32 v226, v226
	v_exp_f32_e32 v178, v178
	s_waitcnt lgkmcnt(2)
	v_mfma_f32_32x32x16_f16 v[98:113], v[4:7], v[118:121], v[98:113]
	ds_read_b128 v[188:191], v173 offset:8320
	ds_read_b128 v[4:7], v174
	ds_read_b128 v[194:197], v174 offset:128
	ds_read_b128 v[198:201], v174 offset:8192
	ds_read_b128 v[202:205], v174 offset:8320
	ds_read_b128 v[206:209], v175
	ds_read_b128 v[210:213], v175 offset:128
	s_waitcnt lgkmcnt(8)
	v_mfma_f32_32x32x16_f16 v[82:97], v[146:149], v[118:121], v[82:97]
	ds_read_b128 v[146:149], v175 offset:8192
	ds_read_b128 v[214:217], v175 offset:8320
	s_waitcnt lgkmcnt(7)
	v_mfma_f32_32x32x16_f16 v[98:113], v[4:7], v[122:125], v[98:113]
	v_add_f32_e32 v4, 0, v230
	v_add_f32_e32 v4, v231, v4
	v_add_f32_e32 v4, v232, v4
	v_add_f32_e32 v4, v233, v4
	v_add_f32_e32 v4, v234, v4
	v_add_f32_e32 v4, v235, v4
	v_add_f32_e32 v4, v236, v4
	s_waitcnt lgkmcnt(5)
	v_mfma_f32_32x32x16_f16 v[82:97], v[198:201], v[122:125], v[82:97]
	v_add_f32_e32 v4, v237, v4
	v_add_f32_e32 v4, v238, v4
	v_add_f32_e32 v4, v239, v4
	v_add_f32_e32 v4, v240, v4
	v_add_f32_e32 v4, v241, v4
	v_add_f32_e32 v4, v242, v4
	v_add_f32_e32 v4, v243, v4
	s_waitcnt lgkmcnt(3)
	v_mfma_f32_32x32x16_f16 v[98:113], v[206:209], v[126:129], v[98:113]
	v_add_f32_e32 v4, v244, v4
	v_add_f32_e32 v4, v245, v4
	v_add_f32_e32 v4, v183, v4
	v_add_f32_e32 v4, v246, v4
	v_add_f32_e32 v4, v247, v4
	v_add_f32_e32 v4, v218, v4
	v_add_f32_e32 v4, v219, v4
	s_waitcnt lgkmcnt(1)
	v_mfma_f32_32x32x16_f16 v[82:97], v[146:149], v[126:129], v[82:97]
	v_add_f32_e32 v4, v220, v4
	v_add_f32_e32 v4, v221, v4
	v_add_f32_e32 v4, v222, v4
	v_exp_f32_e32 v198, v227
	v_add_f32_e32 v4, v223, v4
	v_exp_f32_e32 v199, v228
	v_add_f32_e32 v4, v224, v4
	v_mfma_f32_32x32x16_f16 v[98:113], v[8:11], v[130:133], v[98:113]
	v_exp_f32_e32 v200, v229
	v_add_f32_e32 v4, v225, v4
	v_add_f32_e32 v4, v226, v4
	v_add_f32_e32 v4, v198, v4
	v_add_f32_e32 v4, v199, v4
	v_add_f32_e32 v4, v200, v4
	v_add_f32_e32 v192, v178, v4
	v_mfma_f32_32x32x16_f16 v[82:97], v[12:15], v[130:133], v[82:97]
	v_mov_b32_e32 v193, v192
	v_cvt_pk_f16_f32 v4, v230, v231
	v_cvt_pk_f16_f32 v5, v232, v233
	v_cvt_pk_f16_f32 v6, v234, v235
	v_cvt_pk_f16_f32 v7, v236, v237
	v_cvt_pk_f16_f32 v8, v238, v239
	v_cvt_pk_f16_f32 v9, v240, v241
	v_mfma_f32_32x32x16_f16 v[98:113], v[184:187], v[134:137], v[98:113]
	v_cvt_pk_f16_f32 v10, v242, v243
	v_cvt_pk_f16_f32 v11, v244, v245
	v_cvt_pk_f16_f32 v12, v183, v246
	v_cvt_pk_f16_f32 v13, v247, v218
	v_cvt_pk_f16_f32 v14, v219, v220
	v_cvt_pk_f16_f32 v15, v221, v222
	v_cvt_pk_f16_f32 v146, v223, v224
	v_mfma_f32_32x32x16_f16 v[82:97], v[188:191], v[134:137], v[82:97]
	v_cvt_pk_f16_f32 v147, v225, v226
	v_cvt_pk_f16_f32 v148, v198, v199
	v_cvt_pk_f16_f32 v149, v200, v178
	v_permlane32_swap_b32_e32 v192, v193
	v_permlane32_swap_b32_e32 v4, v6
	v_mfma_f32_32x32x16_f16 v[98:113], v[194:197], v[138:141], v[98:113]
	v_permlane32_swap_b32_e32 v5, v7
	v_permlane32_swap_b32_e32 v8, v10
	v_permlane32_swap_b32_e32 v9, v11
	v_permlane32_swap_b32_e32 v12, v14
	v_mfma_f32_32x32x16_f16 v[82:97], v[202:205], v[138:141], v[82:97]
	v_permlane32_swap_b32_e32 v13, v15
	v_permlane32_swap_b32_e32 v146, v148
	v_permlane32_swap_b32_e32 v147, v149
	v_mfma_f32_32x32x16_f16 v[98:113], v[210:213], v[142:145], v[98:113]
	s_waitcnt lgkmcnt(0)
	v_mfma_f32_32x32x16_f16 v[82:97], v[214:217], v[142:145], v[82:97]
	s_add_i32 s72, s72, 2
	s_cmp_gt_u32 s72, s83
	s_cbranch_scc1 .LBB1_20
	s_add_u32 s4, s74, 0x18000
	s_addc_u32 s5, s75, 0
	s_add_i32 m0, s69, 0x18000
	s_nop 0
	global_load_lds_dwordx4 v154, s[4:5]
	s_add_i32 m0, s69, 0x1a000
	s_nop 0
	global_load_lds_dwordx4 v250, s[4:5]
	s_add_i32 m0, s69, 0x1c000
	s_nop 0
	global_load_lds_dwordx4 v251, s[4:5]
	s_add_i32 m0, s69, 0x1e000
	s_nop 0
	global_load_lds_dwordx4 v252, s[4:5]
.LBB1_20:
	s_add_u32 s6, s76, 0x10000
	s_addc_u32 s7, s77, 0
	s_mov_b32 m0, s69
	s_nop 0
	global_load_lds_dwordx4 v154, s[6:7]
	s_add_i32 m0, s69, 0x2000
	s_nop 0
	global_load_lds_dwordx4 v250, s[6:7]
	s_add_i32 m0, s69, 0x4000
	s_nop 0
	global_load_lds_dwordx4 v251, s[6:7]
	s_add_i32 m0, s69, 0x6000
	s_nop 0
	global_load_lds_dwordx4 v252, s[6:7]
	s_cmp_le_i32 s68, s93
	s_cbranch_scc1 .LBB1_22
	v_cmp_gt_i32_e64 s[62:63], 26, v179
	v_cmp_gt_i32_e64 s[64:65], 27, v179
	v_cmp_gt_i32_e64 s[60:61], 25, v179
	s_and_b64 s[62:63], s[64:65], s[62:63]
	v_cmp_gt_i32_e64 s[58:59], 24, v179
	s_and_b64 s[60:61], s[62:63], s[60:61]
	v_cmp_gt_i32_e64 s[56:57], 19, v179
	s_and_b64 s[58:59], s[60:61], s[58:59]
	v_cmp_gt_i32_e64 s[54:55], 18, v179
	s_and_b64 s[56:57], s[58:59], s[56:57]
	v_cmp_gt_i32_e64 s[52:53], 17, v179
	s_and_b64 s[54:55], s[56:57], s[54:55]
	v_cmp_gt_i32_e64 s[50:51], 16, v179
	s_and_b64 s[52:53], s[54:55], s[52:53]
	v_cmp_gt_i32_e64 s[48:49], 11, v179
	s_and_b64 s[50:51], s[52:53], s[50:51]
	v_cmp_gt_i32_e64 s[46:47], 10, v179
	s_and_b64 s[48:49], s[50:51], s[48:49]
	v_cmp_gt_i32_e64 s[44:45], 9, v179
	s_and_b64 s[46:47], s[48:49], s[46:47]
	v_cmp_gt_i32_e64 s[42:43], 8, v179
	s_and_b64 s[44:45], s[46:47], s[44:45]
	v_cmp_gt_i32_e64 s[40:41], 3, v179
	s_and_b64 s[42:43], s[44:45], s[42:43]
	v_cmp_gt_i32_e64 s[38:39], 2, v179
	s_and_b64 s[40:41], s[42:43], s[40:41]
	v_cmp_gt_i32_e64 s[36:37], 1, v179
	s_and_b64 s[38:39], s[40:41], s[38:39]
	v_cmp_gt_i32_e64 s[34:35], 0, v179
	s_and_b64 s[36:37], s[38:39], s[36:37]
	s_and_b64 s[34:35], s[36:37], s[34:35]
	v_cmp_gt_i32_e64 s[30:31], 58, v179
	v_cndmask_b32_e64 v98, v98, v164, s[34:35]
	v_cmp_gt_i32_e64 s[34:35], 59, v179
	v_cmp_gt_i32_e64 s[28:29], 57, v179
	s_and_b64 s[30:31], s[34:35], s[30:31]
	v_cmp_gt_i32_e64 s[26:27], 56, v179
	s_and_b64 s[28:29], s[30:31], s[28:29]
	v_cmp_gt_i32_e64 s[24:25], 51, v179
	s_and_b64 s[26:27], s[28:29], s[26:27]
	v_cmp_gt_i32_e64 s[22:23], 50, v179
	s_and_b64 s[24:25], s[26:27], s[24:25]
	v_cmp_gt_i32_e64 s[20:21], 49, v179
	s_and_b64 s[22:23], s[24:25], s[22:23]
	v_cmp_gt_i32_e64 s[18:19], 48, v179
	s_and_b64 s[20:21], s[22:23], s[20:21]
	v_cmp_gt_i32_e64 s[16:17], 43, v179
	s_and_b64 s[18:19], s[20:21], s[18:19]
	v_cmp_gt_i32_e64 s[14:15], 42, v179
	s_and_b64 s[16:17], s[18:19], s[16:17]
	v_cmp_gt_i32_e64 s[12:13], 41, v179
	s_and_b64 s[14:15], s[16:17], s[14:15]
	v_cmp_gt_i32_e64 s[10:11], 40, v179
	s_and_b64 s[12:13], s[14:15], s[12:13]
	v_cmp_gt_i32_e64 s[8:9], 35, v179
	s_and_b64 s[10:11], s[12:13], s[10:11]
	v_cmp_gt_i32_e64 s[6:7], 34, v179
	s_and_b64 s[8:9], s[10:11], s[8:9]
	v_cmp_gt_i32_e64 s[4:5], 33, v179
	s_and_b64 s[6:7], s[8:9], s[6:7]
	v_cmp_gt_i32_e32 vcc, 32, v179
	s_and_b64 s[4:5], s[6:7], s[4:5]
	s_and_b64 vcc, s[4:5], vcc
	v_cndmask_b32_e64 v113, v113, v164, s[64:65]
	v_cndmask_b32_e64 v112, v112, v164, s[62:63]
	v_cndmask_b32_e64 v111, v111, v164, s[60:61]
	v_cndmask_b32_e64 v110, v110, v164, s[58:59]
	v_cndmask_b32_e64 v109, v109, v164, s[56:57]
	v_cndmask_b32_e64 v108, v108, v164, s[54:55]
	v_cndmask_b32_e64 v107, v107, v164, s[52:53]
	v_cndmask_b32_e64 v106, v106, v164, s[50:51]
	v_cndmask_b32_e64 v105, v105, v164, s[48:49]
	v_cndmask_b32_e64 v104, v104, v164, s[46:47]
	v_cndmask_b32_e64 v103, v103, v164, s[44:45]
	v_cndmask_b32_e64 v102, v102, v164, s[42:43]
	v_cndmask_b32_e64 v101, v101, v164, s[40:41]
	v_cndmask_b32_e64 v100, v100, v164, s[38:39]
	v_cndmask_b32_e64 v99, v99, v164, s[36:37]
	v_cndmask_b32_e64 v97, v97, v164, s[34:35]
	v_cndmask_b32_e64 v96, v96, v164, s[30:31]
	v_cndmask_b32_e64 v95, v95, v164, s[28:29]
	v_cndmask_b32_e64 v94, v94, v164, s[26:27]
	v_cndmask_b32_e64 v93, v93, v164, s[24:25]
	v_cndmask_b32_e64 v92, v92, v164, s[22:23]
	v_cndmask_b32_e64 v91, v91, v164, s[20:21]
	v_cndmask_b32_e64 v90, v90, v164, s[18:19]
	v_cndmask_b32_e64 v89, v89, v164, s[16:17]
	v_cndmask_b32_e64 v88, v88, v164, s[14:15]
	v_cndmask_b32_e64 v87, v87, v164, s[12:13]
	v_cndmask_b32_e64 v86, v86, v164, s[10:11]
	v_cndmask_b32_e64 v85, v85, v164, s[8:9]
	v_cndmask_b32_e64 v84, v84, v164, s[6:7]
	v_cndmask_b32_e64 v83, v83, v164, s[4:5]
	v_cndmask_b32_e32 v82, v82, v164, vcc

	.amdhsa_kernel _Z11attn_kernelPKDF16_S0_S0_PDF16_PKfS1_
		.amdhsa_group_segment_fixed_size 0
		.amdhsa_private_segment_fixed_size 0
		.amdhsa_kernarg_size 48
		.amdhsa_user_sgpr_count 2
		.amdhsa_user_sgpr_dispatch_ptr 0
		.amdhsa_user_sgpr_queue_ptr 0
		.amdhsa_user_sgpr_kernarg_segment_ptr 1
		.amdhsa_user_sgpr_dispatch_id 0
		.amdhsa_user_sgpr_kernarg_preload_length 0
		.amdhsa_user_sgpr_kernarg_preload_offset 0
		.amdhsa_user_sgpr_private_segment_size 0
		.amdhsa_uses_dynamic_stack 0
		.amdhsa_enable_private_segment 0
		.amdhsa_system_sgpr_workgroup_id_x 1
		.amdhsa_system_sgpr_workgroup_id_y 0
		.amdhsa_system_sgpr_workgroup_id_z 0
		.amdhsa_system_sgpr_workgroup_info 0
		.amdhsa_system_vgpr_workitem_id 0
		.amdhsa_next_free_vgpr 253
		.amdhsa_next_free_sgpr 100
		.amdhsa_accum_offset 256
		.amdhsa_reserve_vcc 1
		.amdhsa_float_round_mode_32 0
		.amdhsa_float_round_mode_16_64 0
		.amdhsa_float_denorm_mode_32 3
		.amdhsa_float_denorm_mode_16_64 3
		.amdhsa_dx10_clamp 1
		.amdhsa_ieee_mode 1
		.amdhsa_fp16_overflow 0
		.amdhsa_tg_split 0
		.amdhsa_exception_fp_ieee_invalid_op 0
		.amdhsa_exception_fp_denorm_src 0
		.amdhsa_exception_fp_ieee_div_zero 0
		.amdhsa_exception_fp_ieee_overflow 0
		.amdhsa_exception_fp_ieee_underflow 0
		.amdhsa_exception_fp_ieee_inexact 0
		.amdhsa_exception_int_div_zero 0
	.end_amdhsa_kernel

_Z13k_gemm_a1b2x3IN3pg87EpiF32WEEvNS0_4GemmET_:
	s_load_dword s8, s[0:1], 0x18
	s_load_dwordx4 s[4:7], s[0:1], 0x0
	s_load_dwordx4 s[24:27], s[0:1], 0x20
	s_load_dword s28, s[0:1], 0x30
	s_lshl_b32 s3, s2, 2
	s_and_b32 s10, s3, 24
	s_bfe_u32 s11, s2, 0x30003
	s_waitcnt lgkmcnt(0)
	s_ashr_i32 s9, s8, 31
	s_or_b32 s10, s10, s11
	s_and_b32 s11, s3, 4
	s_ashr_i32 s2, s2, 6
	s_add_i32 s11, s11, s2
	s_lshr_b32 s2, s9, 27
	v_readfirstlane_b32 s12, v0
	s_add_i32 s2, s8, s2
	s_ashr_i32 s2, s2, 5
	s_lshr_b32 s14, s12, 7
	v_and_b32_e32 v1, 63, v0
	s_bfe_u32 s3, s12, 0x10006
	s_mul_i32 s14, s14, s2
	s_lshr_b32 s13, s12, 6
	v_lshlrev_b32_e32 v66, 4, v1
	s_add_i32 s14, s14, s3
	v_lshl_or_b32 v68, s14, 10, v66
	s_add_i32 s14, s13, 8
	s_lshr_b32 s14, s14, 1
	s_mul_i32 s2, s14, s2
	s_add_i32 s2, s2, s3
	v_lshl_or_b32 v70, s2, 10, v66
	s_lshl_b64 s[2:3], s[8:9], 8
	s_lshr_b64 s[16:17], s[8:9], 24
	s_mul_i32 s16, s16, s10
	s_mul_hi_u32 s17, s2, s10
	s_lshr_b32 s15, s12, 8
	s_lshl_b32 s14, s13, 10
	s_add_i32 s17, s17, s16
	s_mul_i32 s16, s2, s10
	s_add_u32 s4, s4, s16
	s_addc_u32 s5, s5, s17
	s_add_i32 s14, s14, 0
	s_mul_hi_i32 s17, s11, s8
	s_mul_i32 s16, s11, s8
	s_lshl_b32 s29, s11, 10
	s_add_u32 s30, s26, s29
	s_addc_u32 s31, s27, 0
	v_lshrrev_b32_e32 v124, 2, v0
	v_and_b32_e32 v124, 12, v124
	s_lshl_b32 s29, s13, 5
	s_and_b32 s29, s29, 0x60
	v_or_b32_e32 v124, s29, v124
	v_lshlrev_b32_e32 v124, 2, v124
	global_load_dwordx4 v[128:131], v124, s[30:31]
	global_load_dwordx4 v[132:135], v124, s[30:31] offset:64
	global_load_dwordx4 v[136:139], v124, s[30:31] offset:512
	global_load_dwordx4 v[140:143], v124, s[30:31] offset:576
	s_mov_b32 m0, s14
	s_lshl_b64 s[16:17], s[16:17], 9
	global_load_lds_dwordx4 v68, s[4:5]
	s_add_i32 m0, s14, 0x2000
	s_add_u32 s6, s6, s16
	global_load_lds_dwordx4 v70, s[4:5]
	s_addc_u32 s7, s7, s17
	s_add_i32 m0, s14, 0x4000
	v_mov_b32_e32 v69, 0
	global_load_lds_dwordx4 v68, s[6:7]
	s_add_i32 m0, s14, 0x6000
	s_add_u32 s16, s6, s2
	global_load_lds_dwordx4 v70, s[6:7]
	s_addc_u32 s17, s7, s3
	s_add_i32 m0, s14, 0x8000
	v_mov_b32_e32 v71, v69
	global_load_lds_dwordx4 v68, s[16:17]
	s_add_i32 m0, s14, 0xa000
	v_lshl_add_u64 v[12:13], s[4:5], 0, v[68:69]
	global_load_lds_dwordx4 v70, s[16:17]
	v_lshl_add_u64 v[10:11], s[4:5], 0, v[70:71]
	v_lshl_add_u64 v[8:9], s[6:7], 0, v[68:69]
	v_lshl_add_u64 v[6:7], s[6:7], 0, v[70:71]
	v_lshl_add_u64 v[4:5], s[16:17], 0, v[68:69]
	s_cmp_lg_u32 s15, 1
	v_lshl_add_u64 v[2:3], s[16:17], 0, v[70:71]
	s_cbranch_scc1 .LBB3_2
	s_barrier

.LBB3_6:
	s_mov_b64 s[4:5], s[24:25]
	s_mov_b64 s[6:7], s[26:27]
	s_mov_b32 s8, s28
	s_waitcnt vmcnt(0)
	s_cmpk_lt_u32 s12, 0x100
	s_cbranch_scc0 .LBB3_8
	s_barrier
.LBB3_8:
	s_lshl_b32 s0, s11, 8
	s_ashr_i32 s1, s0, 31
	v_lshrrev_b32_e32 v5, 2, v0
	s_lshl_b64 s[0:1], s[0:1], 2
	v_and_or_b32 v5, v5, 12, s13
	s_waitcnt lgkmcnt(0)
	s_add_u32 s2, s6, s0
	s_addc_u32 s3, s7, s1
	v_lshlrev_b32_e32 v68, 2, v5
	s_barrier
	s_movk_i32 s2, 0x410
	v_mov_b32_e32 v5, v69
	v_add_u32_e32 v88, 0, v66
	v_lshrrev_b32_e32 v69, 6, v0
	v_or_b32_e32 v86, 0x200, v0
	v_mul_lo_u32 v1, v1, s2
	v_mad_u32_u24 v89, v69, s2, v88
	v_lshrrev_b32_e32 v86, 6, v86
	v_add3_u32 v1, 0, v68, v1
	s_lshl_b32 s3, s10, 7
	v_mad_u32_u24 v90, v86, s2, v88
	v_or_b32_e32 v91, s3, v69
	v_or_b32_e32 v86, s3, v86
	v_mad_i64_i32 v[68:69], s[6:7], s8, v91, 0
	v_mad_i64_i32 v[86:87], s[6:7], s8, v86, 0
	v_lshl_add_u64 v[68:69], v[68:69], 2, s[4:5]
	v_lshl_add_u64 v[86:87], v[86:87], 2, s[4:5]
	v_mov_b32_e32 v67, 0
	v_lshl_add_u64 v[68:69], v[68:69], 0, s[0:1]
	v_lshl_add_u64 v[86:87], v[86:87], 0, s[0:1]
	s_waitcnt vmcnt(0)
	v_pk_add_f32 v[64:65], v[64:65], v[130:131]
	v_pk_add_f32 v[62:63], v[62:63], v[128:129]
	v_pk_add_f32 v[60:61], v[60:61], v[130:131]
	v_pk_add_f32 v[4:5], v[4:5], v[142:143]
	v_pk_add_f32 v[2:3], v[2:3], v[140:141]
	v_pk_add_f32 v[58:59], v[58:59], v[128:129]
	v_pk_add_f32 v[56:57], v[56:57], v[130:131]
	v_pk_add_f32 v[54:55], v[54:55], v[128:129]
	v_pk_add_f32 v[52:53], v[52:53], v[130:131]
	v_pk_add_f32 v[50:51], v[50:51], v[128:129]
	v_pk_add_f32 v[48:49], v[48:49], v[134:135]
	v_pk_add_f32 v[46:47], v[46:47], v[132:133]
	v_pk_add_f32 v[44:45], v[44:45], v[134:135]
	v_pk_add_f32 v[42:43], v[42:43], v[132:133]
	v_pk_add_f32 v[40:41], v[40:41], v[134:135]
	v_pk_add_f32 v[38:39], v[38:39], v[132:133]
	v_pk_add_f32 v[28:29], v[28:29], v[134:135]
	v_pk_add_f32 v[26:27], v[26:27], v[132:133]
	v_pk_add_f32 v[36:37], v[36:37], v[138:139]
	v_pk_add_f32 v[34:35], v[34:35], v[136:137]
	v_pk_add_f32 v[32:33], v[32:33], v[138:139]
	v_pk_add_f32 v[30:31], v[30:31], v[136:137]
	v_pk_add_f32 v[24:25], v[24:25], v[138:139]
	v_pk_add_f32 v[22:23], v[22:23], v[136:137]
	v_pk_add_f32 v[20:21], v[20:21], v[138:139]
	v_pk_add_f32 v[18:19], v[18:19], v[136:137]
	v_pk_add_f32 v[16:17], v[16:17], v[142:143]
	v_pk_add_f32 v[14:15], v[14:15], v[140:141]
	v_pk_add_f32 v[12:13], v[12:13], v[142:143]
	v_pk_add_f32 v[10:11], v[10:11], v[140:141]
	v_pk_add_f32 v[8:9], v[8:9], v[142:143]
	v_pk_add_f32 v[6:7], v[6:7], v[140:141]
	ds_write_b128 v1, v[62:65]
	ds_write_b128 v1, v[58:61] offset:16640
	ds_write_b128 v1, v[54:57] offset:33280
	ds_write_b128 v1, v[50:53] offset:49920
	ds_write_b128 v1, v[46:49] offset:64
	ds_write_b128 v1, v[42:45] offset:16704
	ds_write_b128 v1, v[38:41] offset:33344
	ds_write_b128 v1, v[26:29] offset:49984
	ds_write_b128 v1, v[34:37] offset:512
	ds_write_b128 v1, v[30:33] offset:17152
	ds_write_b128 v1, v[22:25] offset:33792
	ds_write_b128 v1, v[18:21] offset:50432
	ds_write_b128 v1, v[14:17] offset:576
	ds_write_b128 v1, v[10:13] offset:17216
	ds_write_b128 v1, v[6:9] offset:33856
	ds_write_b128 v1, v[2:5] offset:50496
	s_waitcnt lgkmcnt(0)
	s_barrier
	ds_read_b128 v[2:5], v89
	ds_read_b128 v[6:9], v90
	ds_read_b128 v[10:13], v89 offset:16640
	v_lshl_add_u64 v[14:15], v[68:69], 0, v[66:67]
	v_lshl_add_u64 v[16:17], v[86:87], 0, v[66:67]
	v_add_u32_e32 v1, 0x4100, v89
	s_waitcnt lgkmcnt(2)
	global_store_dwordx4 v[14:15], v[2:5], off nt
	s_waitcnt lgkmcnt(1)
	global_store_dwordx4 v[16:17], v[6:9], off nt
	ds_read_b128 v[2:5], v1 offset:49920
	s_nop 0
	v_or_b32_e32 v6, 16, v91
	v_mad_i64_i32 v[6:7], s[6:7], s8, v6, 0
	v_lshl_add_u64 v[6:7], v[6:7], 2, s[4:5]
	v_lshl_add_u64 v[6:7], v[6:7], 0, s[0:1]
	v_lshl_add_u64 v[6:7], v[6:7], 0, v[66:67]
	s_waitcnt lgkmcnt(1)
	global_store_dwordx4 v[6:7], v[10:13], off nt
	v_or_b32_e32 v6, 0x600, v0
	s_nop 0
	v_lshrrev_b32_e32 v10, 6, v6
	v_mad_u32_u24 v6, v10, s2, v88
	ds_read_b128 v[6:9], v6
	v_or_b32_e32 v10, s3, v10
	v_mad_i64_i32 v[10:11], s[6:7], s8, v10, 0
	v_lshl_add_u64 v[10:11], v[10:11], 2, s[4:5]
	v_lshl_add_u64 v[10:11], v[10:11], 0, s[0:1]
	v_lshl_add_u64 v[14:15], v[10:11], 0, v[66:67]
	s_waitcnt lgkmcnt(0)
	global_store_dwordx4 v[14:15], v[6:9], off nt
	ds_read_b128 v[6:9], v89 offset:33280
	v_or_b32_e32 v14, 32, v91
	v_mad_i64_i32 v[14:15], s[6:7], s8, v14, 0
	v_lshl_add_u64 v[14:15], v[14:15], 2, s[4:5]
	v_lshl_add_u64 v[14:15], v[14:15], 0, s[0:1]
	v_lshl_add_u64 v[18:19], v[14:15], 0, v[66:67]
	s_waitcnt lgkmcnt(0)
	global_store_dwordx4 v[18:19], v[6:9], off nt
	v_add_u32_e32 v10, 0x8200, v89
	ds_read_b128 v[10:13], v10 offset:49920
	v_or_b32_e32 v6, 0xa00, v0
	v_lshrrev_b32_e32 v18, 6, v6
	v_mad_u32_u24 v6, v18, s2, v88
	ds_read_b128 v[6:9], v6
	v_or_b32_e32 v18, s3, v18
	v_mad_i64_i32 v[18:19], s[6:7], s8, v18, 0
	v_lshl_add_u64 v[18:19], v[18:19], 2, s[4:5]
	v_lshl_add_u64 v[18:19], v[18:19], 0, s[0:1]
	v_lshl_add_u64 v[22:23], v[18:19], 0, v[66:67]
	ds_read_b128 v[14:17], v89 offset:49920
	s_waitcnt lgkmcnt(1)
	global_store_dwordx4 v[22:23], v[6:9], off nt
	v_add_u32_e32 v18, 0xc300, v89
	ds_read_b128 v[18:21], v18 offset:49920
	v_or_b32_e32 v6, 48, v91
	v_mad_i64_i32 v[6:7], s[6:7], s8, v6, 0
	v_lshl_add_u64 v[6:7], v[6:7], 2, s[4:5]
	v_lshl_add_u64 v[6:7], v[6:7], 0, s[0:1]
	v_lshl_add_u64 v[6:7], v[6:7], 0, v[66:67]
	s_waitcnt lgkmcnt(1)
	global_store_dwordx4 v[6:7], v[14:17], off nt
	v_or_b32_e32 v6, 0xe00, v0
	v_add_u32_e32 v1, 0xc300, v1
	v_lshrrev_b32_e32 v14, 6, v6
	v_mad_u32_u24 v6, v14, s2, v88
	ds_read_b128 v[6:9], v6
	v_or_b32_e32 v14, s3, v14
	v_mad_i64_i32 v[14:15], s[6:7], s8, v14, 0
	v_lshl_add_u64 v[14:15], v[14:15], 2, s[4:5]
	v_lshl_add_u64 v[14:15], v[14:15], 0, s[0:1]
	v_lshl_add_u64 v[22:23], v[14:15], 0, v[66:67]
	ds_read_b128 v[14:17], v1 offset:49920
	v_or_b32_e32 v1, 64, v91
	s_waitcnt lgkmcnt(1)
	global_store_dwordx4 v[22:23], v[6:9], off nt
	s_nop 1
	v_mad_i64_i32 v[6:7], s[6:7], s8, v1, 0
	v_lshl_add_u64 v[6:7], v[6:7], 2, s[4:5]
	v_lshl_add_u64 v[6:7], v[6:7], 0, s[0:1]
	v_or_b32_e32 v1, 0x1200, v0
	v_lshl_add_u64 v[6:7], v[6:7], 0, v[66:67]
	v_lshrrev_b32_e32 v1, 6, v1
	global_store_dwordx4 v[6:7], v[2:5], off nt
	s_nop 1
	v_mad_u32_u24 v2, v1, s2, v88
	ds_read_b128 v[2:5], v2
	v_or_b32_e32 v1, s3, v1
	v_mad_i64_i32 v[6:7], s[6:7], s8, v1, 0
	v_lshl_add_u64 v[6:7], v[6:7], 2, s[4:5]
	v_or_b32_e32 v1, 0x1600, v0
	v_lshl_add_u64 v[6:7], v[6:7], 0, s[0:1]
	v_lshrrev_b32_e32 v1, 6, v1
	v_lshl_add_u64 v[22:23], v[6:7], 0, v[66:67]
	v_mad_u32_u24 v6, v1, s2, v88
	ds_read_b128 v[6:9], v6
	s_waitcnt lgkmcnt(1)
	global_store_dwordx4 v[22:23], v[2:5], off nt
	v_or_b32_e32 v1, s3, v1
	s_nop 0
	v_or_b32_e32 v2, 0x50, v91
	v_mad_i64_i32 v[2:3], s[6:7], s8, v2, 0
	v_lshl_add_u64 v[2:3], v[2:3], 2, s[4:5]
	v_lshl_add_u64 v[2:3], v[2:3], 0, s[0:1]
	v_lshl_add_u64 v[2:3], v[2:3], 0, v[66:67]
	global_store_dwordx4 v[2:3], v[10:13], off nt
	v_mad_i64_i32 v[2:3], s[6:7], s8, v1, 0
	v_lshl_add_u64 v[2:3], v[2:3], 2, s[4:5]
	v_lshl_add_u64 v[2:3], v[2:3], 0, s[0:1]
	v_lshl_add_u64 v[2:3], v[2:3], 0, v[66:67]
	v_or_b32_e32 v1, 0x60, v91
	s_waitcnt lgkmcnt(0)
	global_store_dwordx4 v[2:3], v[6:9], off nt
	v_mad_i64_i32 v[2:3], s[6:7], s8, v1, 0
	v_lshl_add_u64 v[2:3], v[2:3], 2, s[4:5]
	v_lshl_add_u64 v[2:3], v[2:3], 0, s[0:1]
	v_or_b32_e32 v1, 0x1a00, v0
	v_lshl_add_u64 v[2:3], v[2:3], 0, v[66:67]
	v_lshrrev_b32_e32 v1, 6, v1
	global_store_dwordx4 v[2:3], v[18:21], off nt
	v_mad_u32_u24 v2, v1, s2, v88
	v_or_b32_e32 v1, s3, v1
	v_mad_i64_i32 v[6:7], s[6:7], s8, v1, 0
	v_or_b32_e32 v0, 0x1e00, v0
	v_lshl_add_u64 v[6:7], v[6:7], 2, s[4:5]
	v_lshrrev_b32_e32 v12, 6, v0
	v_lshl_add_u64 v[6:7], v[6:7], 0, s[0:1]
	v_mad_u32_u24 v0, v12, s2, v88
	ds_read_b128 v[2:5], v2
	v_lshl_add_u64 v[10:11], v[6:7], 0, v[66:67]
	ds_read_b128 v[6:9], v0
	v_or_b32_e32 v0, 0x70, v91
	v_mad_i64_i32 v[0:1], s[6:7], s8, v0, 0
	v_lshl_add_u64 v[0:1], v[0:1], 2, s[4:5]
	v_lshl_add_u64 v[0:1], v[0:1], 0, s[0:1]
	v_lshl_add_u64 v[0:1], v[0:1], 0, v[66:67]
	s_waitcnt lgkmcnt(1)
	global_store_dwordx4 v[10:11], v[2:5], off nt
	global_store_dwordx4 v[0:1], v[14:17], off nt
	v_or_b32_e32 v0, s3, v12
	v_mad_i64_i32 v[0:1], s[2:3], s8, v0, 0
	v_lshl_add_u64 v[0:1], v[0:1], 2, s[4:5]
	v_lshl_add_u64 v[0:1], v[0:1], 0, s[0:1]
	v_lshl_add_u64 v[0:1], v[0:1], 0, v[66:67]
	s_waitcnt lgkmcnt(0)
	global_store_dwordx4 v[0:1], v[6:9], off nt
	s_endpgm

	.amdhsa_kernel _Z13k_gemm_a1b2x3IN3pg87EpiF32WEEvNS0_4GemmET_
		.amdhsa_group_segment_fixed_size 0
		.amdhsa_private_segment_fixed_size 0
		.amdhsa_kernarg_size 56
		.amdhsa_user_sgpr_count 2
		.amdhsa_user_sgpr_dispatch_ptr 0
		.amdhsa_user_sgpr_queue_ptr 0
		.amdhsa_user_sgpr_kernarg_segment_ptr 1
		.amdhsa_user_sgpr_dispatch_id 0
		.amdhsa_user_sgpr_kernarg_preload_length 0
		.amdhsa_user_sgpr_kernarg_preload_offset 0
		.amdhsa_user_sgpr_private_segment_size 0
		.amdhsa_uses_dynamic_stack 0
		.amdhsa_enable_private_segment 0
		.amdhsa_system_sgpr_workgroup_id_x 1
		.amdhsa_system_sgpr_workgroup_id_y 0
		.amdhsa_system_sgpr_workgroup_id_z 0
		.amdhsa_system_sgpr_workgroup_info 0
		.amdhsa_system_vgpr_workitem_id 0
		.amdhsa_next_free_vgpr 144
		.amdhsa_next_free_sgpr 32
		.amdhsa_accum_offset 144
		.amdhsa_reserve_vcc 0
		.amdhsa_float_round_mode_32 0
		.amdhsa_float_round_mode_16_64 0
		.amdhsa_float_denorm_mode_32 3
		.amdhsa_float_denorm_mode_16_64 3
		.amdhsa_dx10_clamp 1
		.amdhsa_ieee_mode 1
		.amdhsa_fp16_overflow 0
		.amdhsa_tg_split 0
		.amdhsa_exception_fp_ieee_invalid_op 0
		.amdhsa_exception_fp_denorm_src 0
		.amdhsa_exception_fp_ieee_div_zero 0
		.amdhsa_exception_fp_ieee_overflow 0
		.amdhsa_exception_fp_ieee_underflow 0
		.amdhsa_exception_fp_ieee_inexact 0
		.amdhsa_exception_int_div_zero 0
	.end_amdhsa_kernel
